# speedup vs baseline: 1.0064x; 1.0064x over previous
_Z6k_mainPKDF16_PKfS2_S2_PKmPjPfS6_:
	s_load_dwordx8 s[52:59], s[0:1], 0x0
	s_load_dwordx8 s[20:27], s[0:1], 0x20
	v_and_b32_e32 v5, 63, v0
	v_lshlrev_b32_e32 v1, 4, v5
	s_and_b32 s4, s2, 7
	v_lshlrev_b32_e32 v10, 2, v0
	s_waitcnt lgkmcnt(0)
	global_load_dwordx4 v[6:9], v1, s[58:59]
	v_mbcnt_lo_u32_b32 v1, -1, 0
	v_mbcnt_hi_u32_b32 v132, -1, v1
	v_lshl_or_b32 v1, s4, 12, v10
	global_load_dword v55, v1, s[56:57]
	global_load_dword v56, v1, s[56:57] offset:1024
	global_load_dword v63, v1, s[56:57] offset:2048
	global_load_dword v64, v1, s[56:57] offset:3072
	v_readfirstlane_b32 s28, v0
	s_lshl_b32 s3, s2, 5
	s_and_b32 s0, s28, 0xffffffc0
	s_and_b32 s1, s3, 0x7fffff00
	s_add_i32 s0, s0, s1
	v_and_b32_e32 v4, 31, v0
	s_lshl_b32 s29, s4, 6
	s_lshl_b32 s1, s0, 4
	v_or_b32_e32 v42, s0, v4
	s_or_b32 s0, s1, s29
	s_ashr_i32 s1, s0, 31
	s_lshl_b64 s[0:1], s[0:1], 6
	s_waitcnt lgkmcnt(0)
	s_add_u32 s0, s20, s0
	s_addc_u32 s1, s21, s1
	s_lshl_b32 s31, s4, 19
	s_add_u32 s4, s52, s31
	v_mov_b32_e32 v3, 0
	v_lshlrev_b32_e32 v2, 4, v0
	s_addc_u32 s5, s53, 0
	s_movk_i32 s8, 0x2000
	v_lshl_add_u64 v[46:47], s[4:5], 0, v[2:3]
	v_add_co_u32_e32 v44, vcc, s8, v46
	s_movk_i32 s9, 0x4000
	s_nop 0
	v_addc_co_u32_e32 v45, vcc, 0, v47, vcc
	v_add_co_u32_e32 v48, vcc, s9, v46
	s_movk_i32 s10, 0x6000
	s_nop 0
	v_addc_co_u32_e32 v49, vcc, 0, v47, vcc
	v_lshlrev_b32_e32 v11, 10, v0
	v_add_co_u32_e32 v50, vcc, s10, v46
	s_mov_b32 s7, 0x8000
	v_and_b32_e32 v10, 0x8000, v11
	v_and_b32_e32 v11, 64, v132
	v_addc_co_u32_e32 v51, vcc, 0, v47, vcc
	v_lshl_or_b32 v61, v4, 7, v10
	v_add_u32_e32 v62, 64, v11
	global_load_dwordx4 v[10:13], v2, s[4:5]
	v_add_co_u32_e32 v52, vcc, s7, v46
	v_xor_b32_e32 v43, 32, v132
	s_nop 0
	v_addc_co_u32_e32 v53, vcc, 0, v47, vcc
	global_load_dwordx4 v[14:17], v[44:45], off offset:-4096
	global_load_dwordx4 v[18:21], v[44:45], off
	global_load_dwordx4 v[22:25], v[48:49], off offset:-4096
	global_load_dwordx4 v[26:29], v[48:49], off
	global_load_dwordx4 v[30:33], v[50:51], off offset:-4096
	global_load_dwordx4 v[34:37], v[50:51], off
	global_load_dwordx4 v[38:41], v[52:53], off offset:-4096
	v_mov_b32_e32 v220, v42
	v_mov_b32_e32 v221, 0
	s_mov_b64 s[94:95], 0x9000
	v_lshl_add_u64 v[222:223], v[220:221], 2, s[54:55]
	v_lshl_add_u64 v[208:209], s[94:95], 0, v[46:47]
	s_mov_b64 s[94:95], 0xb000
	global_load_dword v216, v[222:223], off
	global_load_dword v217, v[222:223], off offset:128
	global_load_dword v218, v61, s[0:1]
	v_lshl_add_u64 v[210:211], s[94:95], 0, v[46:47]
	s_mov_b64 s[94:95], 0xd000
	global_load_dwordx4 v[176:179], v[208:209], off offset:-4096
	global_load_dwordx4 v[180:183], v[208:209], off
	v_lshl_add_u64 v[212:213], s[94:95], 0, v[46:47]
	s_mov_b64 s[94:95], 0xf000
	global_load_dwordx4 v[184:187], v[210:211], off offset:-4096
	global_load_dwordx4 v[188:191], v[210:211], off
	v_lshl_add_u64 v[214:215], s[94:95], 0, v[46:47]
	global_load_dwordx4 v[192:195], v[212:213], off offset:-4096
	global_load_dwordx4 v[196:199], v[212:213], off
	global_load_dwordx4 v[200:203], v[214:215], off offset:-4096
	global_load_dwordx4 v[204:207], v[214:215], off
	v_cmp_lt_i32_e32 vcc, v43, v62
	s_mov_b32 s6, 0x46000000
	v_lshlrev_b32_e32 v54, 1, v0
	v_or_b32_e32 v57, 0x1b000, v54
	v_or_b32_e32 v58, 0x1b800, v54
	v_or_b32_e32 v59, 0x1b200, v54
	v_or_b32_e32 v60, 0x1ba00, v54
	s_movk_i32 s34, 0x90
	s_mov_b32 s4, 0xf000
	s_mov_b32 s30, 0
	s_mov_b32 s7, 0x3e4ccccd
	s_waitcnt vmcnt(23)
	v_max_f32_e32 v1, v9, v9
	v_max_f32_e32 v8, v8, v8
	v_max_f32_e32 v1, v8, v1
	v_max3_f32 v1, v6, v7, v1
	v_cndmask_b32_e32 v7, v132, v43, vcc
	v_lshlrev_b32_e32 v133, 2, v7
	v_mov_b32_dpp v6, v1 quad_perm:[1,0,3,2] row_mask:0xf bank_mask:0xf bound_ctrl:1
	v_max_f32_e32 v6, v6, v6
	v_max_f32_e32 v1, v1, v6
	v_ashrrev_i32_e32 v43, 31, v42
	v_lshl_add_u64 v[8:9], v[42:43], 2, s[54:55]
	v_mov_b32_dpp v6, v1 quad_perm:[2,3,0,1] row_mask:0xf bank_mask:0xf bound_ctrl:1
	v_max_f32_e32 v6, v6, v6
	v_max_f32_e32 v1, v1, v6
	s_nop 1
	v_mov_b32_dpp v6, v1 row_half_mirror row_mask:0xf bank_mask:0xf bound_ctrl:1
	v_max_f32_e32 v6, v6, v6
	v_max_f32_e32 v1, v1, v6
	s_nop 1
	v_mov_b32_dpp v6, v1 row_mirror row_mask:0xf bank_mask:0xf bound_ctrl:1
	v_max_f32_e32 v6, v6, v6
	v_max_f32_e32 v1, v1, v6
	ds_swizzle_b32 v6, v1 offset:swizzle(SWAP,16)
	s_waitcnt lgkmcnt(0)
	v_max_f32_e32 v6, v6, v6
	v_max_f32_e32 v7, v1, v6
	ds_bpermute_b32 v44, v133, v7
	s_waitcnt lgkmcnt(0)
	v_max_f32_e32 v8, v44, v44
	v_max_f32_e32 v7, v7, v8
	s_waitcnt vmcnt(22)
	v_sub_f32_e32 v8, v55, v7
	s_waitcnt vmcnt(21)
	v_sub_f32_e32 v9, v56, v7
	v_mul_f32_e32 v42, 0x3fb8aa3b, v8
	v_mul_f32_e32 v8, 0x3e4ccccd, v8
	v_mul_f32_e32 v43, 0x3fb8aa3b, v9
	v_mul_f32_e32 v9, 0x3e4ccccd, v9
	v_mul_f32_e32 v8, 0x3fb8aa3b, v8
	v_mul_f32_e32 v9, 0x3fb8aa3b, v9
	v_exp_f32_e32 v8, v8
	v_exp_f32_e32 v42, v42
	v_exp_f32_e32 v9, v9
	v_exp_f32_e32 v43, v43
	v_cvt_f16_f32_e32 v8, v8
	v_fma_mixlo_f16 v42, v42, s6, 0
	v_cvt_f16_f32_e32 v9, v9
	v_fma_mixlo_f16 v43, v43, s6, 0
	ds_write_b16 v57, v42
	ds_write_b16 v59, v43
	ds_write_b16 v58, v8
	ds_write_b16 v60, v9
	s_waitcnt vmcnt(20)
	v_sub_f32_e32 v8, v63, v7
	v_mul_f32_e32 v9, 0x3fb8aa3b, v8
	v_exp_f32_e32 v9, v9
	v_mul_f32_e32 v8, 0x3e4ccccd, v8
	v_or_b32_e32 v42, 0x1b400, v54
	v_mul_f32_e32 v8, 0x3fb8aa3b, v8
	v_fma_mixlo_f16 v9, v9, s6, 0
	ds_write_b16 v42, v9
	s_waitcnt vmcnt(19)
	v_sub_f32_e32 v9, v64, v7
	v_exp_f32_e32 v8, v8
	v_mul_f32_e32 v42, 0x3fb8aa3b, v9
	v_mul_f32_e32 v9, 0x3e4ccccd, v9
	v_mul_f32_e32 v9, 0x3fb8aa3b, v9
	v_exp_f32_e32 v9, v9
	v_cvt_f16_f32_e32 v8, v8
	v_exp_f32_e32 v42, v42
	v_or_b32_e32 v43, 0x1bc00, v54
	v_cvt_f16_f32_e32 v9, v9
	ds_write_b16 v43, v8
	v_fma_mixlo_f16 v8, v42, s6, 0
	v_or_b32_e32 v42, 0x1b600, v54
	ds_write_b16 v42, v8
	v_or_b32_e32 v8, 0x1be00, v54
	ds_write_b16 v8, v9
	v_lshrrev_b32_e32 v8, 3, v0
	v_and_b32_e32 v9, 0x70, v2
	v_lshrrev_b32_e32 v144, 4, v0
	v_and_b32_e32 v144, 7, v144
	v_lshlrev_b32_e32 v144, 4, v144
	v_xor_b32_e32 v9, v9, v144
	v_lshl_add_u32 v144, v8, 7, v9
	v_add_co_u32_e32 v8, vcc, s4, v46
	s_mov_b32 s4, 0xa000
	s_nop 0
	v_addc_co_u32_e32 v9, vcc, 0, v47, vcc
	s_waitcnt vmcnt(18)
	ds_write_b128 v144, v[10:13]
	s_waitcnt vmcnt(17)
	ds_write_b128 v144, v[14:17] offset:4096
	s_waitcnt vmcnt(16)
	ds_write_b128 v144, v[18:21] offset:8192
	s_waitcnt vmcnt(15)
	ds_write_b128 v144, v[22:25] offset:12288
	s_waitcnt vmcnt(14)
	ds_write_b128 v144, v[26:29] offset:16384
	s_waitcnt vmcnt(13)
	ds_write_b128 v144, v[30:33] offset:20480
	s_waitcnt vmcnt(12)
	ds_write_b128 v144, v[34:37] offset:24576
	v_add_co_u32_e32 v20, vcc, s4, v46
	s_mov_b32 s4, 0xc000
	s_nop 0
	v_addc_co_u32_e32 v21, vcc, 0, v47, vcc
	v_add_co_u32_e32 v28, vcc, s4, v46
	s_mov_b32 s4, 0xe000
	s_nop 0
	v_addc_co_u32_e32 v29, vcc, 0, v47, vcc
	v_add_co_u32_e32 v36, vcc, s4, v46
	s_waitcnt vmcnt(11)
	ds_write_b128 v144, v[38:41] offset:28672
	v_addc_co_u32_e32 v37, vcc, 0, v47, vcc
	s_nop 0
	s_nop 0
	v_mov_b32_e32 v36, v3
	v_mov_b32_e32 v37, v3
	v_mov_b32_e32 v38, v3
	v_mov_b32_e32 v39, v3
	s_mov_b32 s4, 0x9e3779b9
	s_waitcnt vmcnt(8)
	v_cmp_eq_u32_e32 vcc, s4, v218
	v_mfma_f32_32x32x16_f16 a[0:15], v[36:39], v[36:39], 0
	v_add_u32_e32 v40, 0x10000, v144
	v_mfma_f32_32x32x16_f16 a[16:31], v[36:39], v[36:39], 0
	s_nop 0
	v_mfma_f32_32x32x16_f16 a[32:47], v[36:39], v[36:39], 0
	s_nop 0
	v_mfma_f32_32x32x16_f16 a[48:63], v[36:39], v[36:39], 0
	s_nop 0
	v_mfma_f32_32x32x16_f16 a[64:79], v[36:39], v[36:39], 0
	s_nop 0
	v_mfma_f32_32x32x16_f16 a[112:127], v[36:39], v[36:39], 0
	s_nop 0
	v_mfma_f32_32x32x16_f16 a[128:143], v[36:39], v[36:39], 0
	s_nop 0
	v_mfma_f32_32x32x16_f16 a[80:95], v[36:39], v[36:39], 0
	s_nop 0
	v_mfma_f32_32x32x16_f16 a[240:255], v[36:39], v[36:39], 0
	s_nop 0
	v_mfma_f32_32x32x16_f16 a[224:239], v[36:39], v[36:39], 0
	s_nop 0
	v_mfma_f32_32x32x16_f16 a[208:223], v[36:39], v[36:39], 0
	s_nop 0
	v_mfma_f32_32x32x16_f16 a[192:207], v[36:39], v[36:39], 0
	s_nop 0
	v_mfma_f32_32x32x16_f16 a[176:191], v[36:39], v[36:39], 0
	s_nop 0
	v_mfma_f32_32x32x16_f16 a[160:175], v[36:39], v[36:39], 0
	s_nop 0
	v_mfma_f32_32x32x16_f16 a[144:159], v[36:39], v[36:39], 0
	s_waitcnt vmcnt(7)
	ds_write_b128 v144, v[176:179] offset:36864
	s_waitcnt vmcnt(6)
	ds_write_b128 v144, v[180:183] offset:40960
	s_waitcnt vmcnt(5)
	ds_write_b128 v144, v[184:187] offset:45056
	s_waitcnt vmcnt(4)
	ds_write_b128 v144, v[188:191] offset:49152
	s_waitcnt vmcnt(3)
	ds_write_b128 v144, v[192:195] offset:53248
	s_waitcnt vmcnt(2)
	ds_write_b128 v144, v[196:199] offset:57344
	s_waitcnt vmcnt(1)
	ds_write_b128 v144, v[200:203] offset:61440
	s_waitcnt vmcnt(0)
	ds_write_b128 v40, v[204:207]
	v_mfma_f32_32x32x16_f16 a[96:111], v[36:39], v[36:39], 0
	s_and_saveexec_b64 s[4:5], vcc
	s_cbranch_execz .LBB1_2
	s_nop 0

.LBB1_3:
	s_waitcnt lgkmcnt(0)
	v_mfma_f32_32x32x16_f16 a[0:15], v[18:21], v[74:77], a[0:15]
	s_add_i32 s31, s30, 1
	s_cmp_lg_u32 s30, 2
	s_cselect_b32 s91, s31, 0
	s_mul_i32 s30, s30, 0x9000
	s_mul_i32 s92, s91, 0x9000
	s_add_i32 s96, s92, 0x9000
	s_cmp_lg_u32 s91, 2
	s_cselect_b32 s96, s96, 0
	s_add_i32 s96, s96, s93
	s_mov_b32 m0, s96
	v_add_u32_e32 v147, s30, v208
	global_load_lds_dwordx4 v164, s[94:95]
	s_add_u32 m0, s96, 0x1000
	v_add_u32_e32 v2, s30, v209
	global_load_lds_dwordx4 v165, s[94:95]
	s_add_u32 m0, s96, 0x2000
	v_add_u32_e32 v3, s30, v210
	global_load_lds_dwordx4 v166, s[94:95]
	s_add_u32 m0, s96, 0x3000
	v_add_u32_e32 v146, s92, v141
	global_load_lds_dwordx4 v167, s[94:95]
	s_add_u32 s30, s35, s20
	s_addc_u32 s31, s84, s21
	s_add_u32 m0, s96, 0x4000
	s_load_dwordx16 s[68:83], s[30:31], 0x80
	global_load_lds_dwordx4 v168, s[94:95]
	s_add_u32 m0, s96, 0x5000
	s_load_dwordx16 s[52:67], s[30:31], 0x8080
	global_load_lds_dwordx4 v169, s[94:95]
	s_add_u32 m0, s96, 0x6000
	ds_read_b128 v[90:93], v145
	global_load_lds_dwordx4 v170, s[94:95]
	s_add_u32 m0, s96, 0x7000
	ds_read_b128 v[82:85], v145 offset:2048
	global_load_lds_dwordx4 v171, s[94:95]
	v_mfma_f32_32x32x16_f16 a[240:255], v[38:41], v[74:77], a[240:255]
	ds_read_b128 v[50:53], v147
	v_pk_mul_f16 v148, v46, v136
	v_pk_mul_f16 v149, v42, v137
	v_pk_mul_f16 v150, v47, v136
	v_pk_mul_f16 v151, v43, v137
	v_mfma_f32_32x32x16_f16 a[16:31], v[18:21], v[126:129], a[16:31]
	ds_read_b128 v[54:57], v147 offset:4096
	v_pk_mul_f16 v152, v48, v136
	v_pk_mul_f16 v153, v44, v137
	v_pk_mul_f16 v154, v49, v136
	v_pk_mul_f16 v155, v45, v137
	v_mfma_f32_32x32x16_f16 a[224:239], v[38:41], v[126:129], a[224:239]
	ds_read_b128 v[58:61], v147 offset:8192
	v_pk_mul_f16 v156, v46, v140
	v_pk_mul_f16 v157, v42, v139
	v_pk_mul_f16 v158, v47, v140
	v_pk_mul_f16 v159, v43, v139
	v_mfma_f32_32x32x16_f16 a[32:47], v[18:21], v[122:125], a[32:47]
	ds_read_b128 v[62:65], v147 offset:12288
	v_pk_mul_f16 v160, v48, v140
	v_pk_mul_f16 v161, v44, v139
	v_pk_mul_f16 v162, v49, v140
	v_pk_mul_f16 v163, v45, v139
	v_mfma_f32_32x32x16_f16 a[208:223], v[38:41], v[122:125], a[208:223]
	ds_read_b128 v[66:69], v147 offset:16384
	v_pk_max_f16 v148, v148, v149
	v_pk_max_f16 v150, v150, v151
	v_pk_max_f16 v152, v152, v153
	v_pk_max_f16 v154, v154, v155
	v_mfma_f32_32x32x16_f16 a[48:63], v[18:21], v[118:121], a[48:63]
	ds_read_b128 v[70:73], v147 offset:20480
	v_pk_max_f16 v156, v156, v157
	v_pk_max_f16 v158, v158, v159
	v_pk_max_f16 v160, v160, v161
	v_pk_max_f16 v162, v162, v163
	v_mfma_f32_32x32x16_f16 a[192:207], v[38:41], v[118:121], a[192:207]
	ds_read_b128 v[78:81], v147 offset:24576
	v_cndmask_b32_e64 v114, v1, v148, s[36:37]
	s_mov_b64 vcc, s[38:39]
	v_cndmask_b32_sdwa v114, v1, v148, vcc dst_sel:WORD_1 dst_unused:UNUSED_PRESERVE src0_sel:WORD_1 src1_sel:WORD_1
	v_cndmask_b32_e64 v115, v1, v150, s[40:41]
	s_mov_b64 vcc, s[42:43]
	v_cndmask_b32_sdwa v115, v1, v150, vcc dst_sel:WORD_1 dst_unused:UNUSED_PRESERVE src0_sel:WORD_1 src1_sel:WORD_1
	v_mfma_f32_32x32x16_f16 a[64:79], v[18:21], v[106:109], a[64:79]
	ds_read_b128 v[102:105], v147 offset:28672
	v_cndmask_b32_e64 v116, v1, v152, s[44:45]
	s_mov_b64 vcc, s[46:47]
	v_cndmask_b32_sdwa v116, v1, v152, vcc dst_sel:WORD_1 dst_unused:UNUSED_PRESERVE src0_sel:WORD_1 src1_sel:WORD_1
	v_cndmask_b32_e64 v117, v1, v154, s[48:49]
	s_mov_b64 vcc, s[50:51]
	v_cndmask_b32_sdwa v117, v1, v154, vcc dst_sel:WORD_1 dst_unused:UNUSED_PRESERVE src0_sel:WORD_1 src1_sel:WORD_1
	v_mfma_f32_32x32x16_f16 a[176:191], v[38:41], v[106:109], a[176:191]
	v_cndmask_b32_e64 v110, v138, v156, s[4:5]
	s_mov_b64 vcc, s[6:7]
	v_cndmask_b32_sdwa v110, v138, v156, vcc dst_sel:WORD_1 dst_unused:UNUSED_PRESERVE src0_sel:WORD_1 src1_sel:WORD_1
	v_cndmask_b32_e64 v111, v138, v158, s[8:9]
	s_mov_b64 vcc, s[10:11]
	v_cndmask_b32_sdwa v111, v138, v158, vcc dst_sel:WORD_1 dst_unused:UNUSED_PRESERVE src0_sel:WORD_1 src1_sel:WORD_1
	v_mfma_f32_32x32x16_f16 a[112:127], v[18:21], v[98:101], a[112:127]
	v_cndmask_b32_e64 v112, v138, v160, s[12:13]
	s_mov_b64 vcc, s[14:15]
	v_cndmask_b32_sdwa v112, v138, v160, vcc dst_sel:WORD_1 dst_unused:UNUSED_PRESERVE src0_sel:WORD_1 src1_sel:WORD_1
	v_cndmask_b32_e64 v113, v138, v162, s[16:17]
	s_mov_b64 vcc, s[18:19]
	v_cndmask_b32_sdwa v113, v138, v162, vcc dst_sel:WORD_1 dst_unused:UNUSED_PRESERVE src0_sel:WORD_1 src1_sel:WORD_1
	v_mfma_f32_32x32x16_f16 a[160:175], v[38:41], v[98:101], a[160:175]
	v_pk_add_f16 v148, v115, v114
	v_pk_add_f16 v149, v116, v117
	v_mfma_f32_32x32x16_f16 a[128:143], v[18:21], v[94:97], a[128:143]
	v_pk_add_f16 v150, v111, v110
	v_pk_add_f16 v151, v112, v113
	v_mfma_f32_32x32x16_f16 a[144:159], v[38:41], v[94:97], a[144:159]
	v_pk_add_f16 v148, v148, v149
	v_pk_add_f16 v150, v150, v151
	v_mfma_f32_32x32x16_f16 a[80:95], v[18:21], v[86:89], a[80:95]
	v_fma_mix_f32 v134, v148, 1.0, v134 op_sel_hi:[1,0,0]
	v_fma_mix_f32 v135, v150, 1.0, v135 op_sel_hi:[1,0,0]
	v_mfma_f32_32x32x16_f16 a[96:111], v[38:41], v[86:89], a[96:111]
	v_fma_mix_f32 v134, v148, 1.0, v134 op_sel:[1,0,0] op_sel_hi:[1,0,0]
	v_fma_mix_f32 v135, v150, 1.0, v135 op_sel:[1,0,0] op_sel_hi:[1,0,0]
	s_waitcnt lgkmcnt(0)
	v_mfma_f32_32x32x16_f16 a[0:15], v[114:117], v[50:53], a[0:15]
	s_load_dwordx16 s[36:51], s[30:31], 0xc0
	s_load_dwordx16 s[4:19], s[30:31], 0x80c0
	ds_read_b128 v[46:49], v145 offset:32
	ds_read_b128 v[42:45], v145 offset:2080
	v_mfma_f32_32x32x16_f16 a[240:255], v[110:113], v[50:53], a[240:255]
	ds_read_b128 v[74:77], v2
	v_pk_mul_f16 v148, v90, v136
	v_pk_mul_f16 v149, v82, v137
	v_pk_mul_f16 v150, v91, v136
	v_pk_mul_f16 v151, v83, v137
	v_mfma_f32_32x32x16_f16 a[16:31], v[114:117], v[54:57], a[16:31]
	ds_read_b128 v[126:129], v2 offset:4096
	v_pk_mul_f16 v152, v92, v136
	v_pk_mul_f16 v153, v84, v137
	v_pk_mul_f16 v154, v93, v136
	v_pk_mul_f16 v155, v85, v137
	v_mfma_f32_32x32x16_f16 a[224:239], v[110:113], v[54:57], a[224:239]
	ds_read_b128 v[122:125], v2 offset:8192
	v_pk_mul_f16 v156, v90, v140
	v_pk_mul_f16 v157, v82, v139
	v_pk_mul_f16 v158, v91, v140
	v_pk_mul_f16 v159, v83, v139
	v_mfma_f32_32x32x16_f16 a[32:47], v[114:117], v[58:61], a[32:47]
	ds_read_b128 v[118:121], v2 offset:12288
	v_pk_mul_f16 v160, v92, v140
	v_pk_mul_f16 v161, v84, v139
	v_pk_mul_f16 v162, v93, v140
	v_pk_mul_f16 v163, v85, v139
	v_mfma_f32_32x32x16_f16 a[208:223], v[110:113], v[58:61], a[208:223]
	ds_read_b128 v[106:109], v2 offset:16384
	v_pk_max_f16 v148, v148, v149
	v_pk_max_f16 v150, v150, v151
	v_pk_max_f16 v152, v152, v153
	v_pk_max_f16 v154, v154, v155
	v_mfma_f32_32x32x16_f16 a[48:63], v[114:117], v[62:65], a[48:63]
	ds_read_b128 v[98:101], v2 offset:20480
	v_pk_max_f16 v156, v156, v157
	v_pk_max_f16 v158, v158, v159
	v_pk_max_f16 v160, v160, v161
	v_pk_max_f16 v162, v162, v163
	v_mfma_f32_32x32x16_f16 a[192:207], v[110:113], v[62:65], a[192:207]
	ds_read_b128 v[94:97], v2 offset:24576
	v_cndmask_b32_e64 v18, v1, v148, s[68:69]
	s_mov_b64 vcc, s[70:71]
	v_cndmask_b32_sdwa v18, v1, v148, vcc dst_sel:WORD_1 dst_unused:UNUSED_PRESERVE src0_sel:WORD_1 src1_sel:WORD_1
	v_cndmask_b32_e64 v19, v1, v150, s[72:73]
	s_mov_b64 vcc, s[74:75]
	v_cndmask_b32_sdwa v19, v1, v150, vcc dst_sel:WORD_1 dst_unused:UNUSED_PRESERVE src0_sel:WORD_1 src1_sel:WORD_1
	v_mfma_f32_32x32x16_f16 a[64:79], v[114:117], v[66:69], a[64:79]
	ds_read_b128 v[86:89], v2 offset:28672
	v_cndmask_b32_e64 v20, v1, v152, s[76:77]
	s_mov_b64 vcc, s[78:79]
	v_cndmask_b32_sdwa v20, v1, v152, vcc dst_sel:WORD_1 dst_unused:UNUSED_PRESERVE src0_sel:WORD_1 src1_sel:WORD_1
	v_cndmask_b32_e64 v21, v1, v154, s[80:81]
	s_mov_b64 vcc, s[82:83]
	v_cndmask_b32_sdwa v21, v1, v154, vcc dst_sel:WORD_1 dst_unused:UNUSED_PRESERVE src0_sel:WORD_1 src1_sel:WORD_1
	v_mfma_f32_32x32x16_f16 a[176:191], v[110:113], v[66:69], a[176:191]
	v_cndmask_b32_e64 v38, v138, v156, s[52:53]
	s_mov_b64 vcc, s[54:55]
	v_cndmask_b32_sdwa v38, v138, v156, vcc dst_sel:WORD_1 dst_unused:UNUSED_PRESERVE src0_sel:WORD_1 src1_sel:WORD_1
	v_cndmask_b32_e64 v39, v138, v158, s[56:57]
	s_mov_b64 vcc, s[58:59]
	v_cndmask_b32_sdwa v39, v138, v158, vcc dst_sel:WORD_1 dst_unused:UNUSED_PRESERVE src0_sel:WORD_1 src1_sel:WORD_1
	v_mfma_f32_32x32x16_f16 a[112:127], v[114:117], v[70:73], a[112:127]
	v_cndmask_b32_e64 v40, v138, v160, s[60:61]
	s_mov_b64 vcc, s[62:63]
	v_cndmask_b32_sdwa v40, v138, v160, vcc dst_sel:WORD_1 dst_unused:UNUSED_PRESERVE src0_sel:WORD_1 src1_sel:WORD_1
	v_cndmask_b32_e64 v41, v138, v162, s[64:65]
	s_mov_b64 vcc, s[66:67]
	v_cndmask_b32_sdwa v41, v138, v162, vcc dst_sel:WORD_1 dst_unused:UNUSED_PRESERVE src0_sel:WORD_1 src1_sel:WORD_1
	v_mfma_f32_32x32x16_f16 a[160:175], v[110:113], v[70:73], a[160:175]
	v_pk_add_f16 v148, v19, v18
	v_pk_add_f16 v149, v20, v21
	v_mfma_f32_32x32x16_f16 a[128:143], v[114:117], v[78:81], a[128:143]
	v_pk_add_f16 v150, v39, v38
	v_pk_add_f16 v151, v40, v41
	v_mfma_f32_32x32x16_f16 a[144:159], v[110:113], v[78:81], a[144:159]
	v_pk_add_f16 v148, v148, v149
	v_pk_add_f16 v150, v150, v151
	v_mfma_f32_32x32x16_f16 a[80:95], v[114:117], v[102:105], a[80:95]
	v_fma_mix_f32 v134, v148, 1.0, v134 op_sel_hi:[1,0,0]
	v_fma_mix_f32 v135, v150, 1.0, v135 op_sel_hi:[1,0,0]
	v_mfma_f32_32x32x16_f16 a[96:111], v[110:113], v[102:105], a[96:111]
	v_fma_mix_f32 v134, v148, 1.0, v134 op_sel:[1,0,0] op_sel_hi:[1,0,0]
	v_fma_mix_f32 v135, v150, 1.0, v135 op_sel:[1,0,0] op_sel_hi:[1,0,0]
	s_waitcnt lgkmcnt(0)
	v_mfma_f32_32x32x16_f16 a[0:15], v[18:21], v[74:77], a[0:15]
	s_load_dwordx16 s[68:83], s[30:31], 0x100
	s_load_dwordx16 s[52:67], s[30:31], 0x8100
	ds_read_b128 v[90:93], v145 offset:64
	ds_read_b128 v[82:85], v145 offset:2112
	v_mfma_f32_32x32x16_f16 a[240:255], v[38:41], v[74:77], a[240:255]
	ds_read_b128 v[50:53], v3
	v_pk_mul_f16 v148, v46, v136
	v_pk_mul_f16 v149, v42, v137
	v_pk_mul_f16 v150, v47, v136
	v_pk_mul_f16 v151, v43, v137
	v_mfma_f32_32x32x16_f16 a[16:31], v[18:21], v[126:129], a[16:31]
	ds_read_b128 v[54:57], v3 offset:4096
	v_pk_mul_f16 v152, v48, v136
	v_pk_mul_f16 v153, v44, v137
	v_pk_mul_f16 v154, v49, v136
	v_pk_mul_f16 v155, v45, v137
	v_mfma_f32_32x32x16_f16 a[224:239], v[38:41], v[126:129], a[224:239]
	ds_read_b128 v[58:61], v3 offset:8192
	v_pk_mul_f16 v156, v46, v140
	v_pk_mul_f16 v157, v42, v139
	v_pk_mul_f16 v158, v47, v140
	v_pk_mul_f16 v159, v43, v139
	v_mfma_f32_32x32x16_f16 a[32:47], v[18:21], v[122:125], a[32:47]
	ds_read_b128 v[62:65], v3 offset:12288
	v_pk_mul_f16 v160, v48, v140
	v_pk_mul_f16 v161, v44, v139
	v_pk_mul_f16 v162, v49, v140
	v_pk_mul_f16 v163, v45, v139
	v_mfma_f32_32x32x16_f16 a[208:223], v[38:41], v[122:125], a[208:223]
	ds_read_b128 v[66:69], v3 offset:16384
	v_pk_max_f16 v148, v148, v149
	v_pk_max_f16 v150, v150, v151
	v_pk_max_f16 v152, v152, v153
	v_pk_max_f16 v154, v154, v155
	v_mfma_f32_32x32x16_f16 a[48:63], v[18:21], v[118:121], a[48:63]
	ds_read_b128 v[70:73], v3 offset:20480
	v_pk_max_f16 v156, v156, v157
	v_pk_max_f16 v158, v158, v159
	v_pk_max_f16 v160, v160, v161
	v_pk_max_f16 v162, v162, v163
	v_mfma_f32_32x32x16_f16 a[192:207], v[38:41], v[118:121], a[192:207]
	ds_read_b128 v[78:81], v3 offset:24576
	v_cndmask_b32_e64 v114, v1, v148, s[36:37]
	s_mov_b64 vcc, s[38:39]
	v_cndmask_b32_sdwa v114, v1, v148, vcc dst_sel:WORD_1 dst_unused:UNUSED_PRESERVE src0_sel:WORD_1 src1_sel:WORD_1
	v_cndmask_b32_e64 v115, v1, v150, s[40:41]
	s_mov_b64 vcc, s[42:43]
	v_cndmask_b32_sdwa v115, v1, v150, vcc dst_sel:WORD_1 dst_unused:UNUSED_PRESERVE src0_sel:WORD_1 src1_sel:WORD_1
	v_mfma_f32_32x32x16_f16 a[64:79], v[18:21], v[106:109], a[64:79]
	ds_read_b128 v[102:105], v3 offset:28672
	v_cndmask_b32_e64 v116, v1, v152, s[44:45]
	s_mov_b64 vcc, s[46:47]
	v_cndmask_b32_sdwa v116, v1, v152, vcc dst_sel:WORD_1 dst_unused:UNUSED_PRESERVE src0_sel:WORD_1 src1_sel:WORD_1
	v_cndmask_b32_e64 v117, v1, v154, s[48:49]
	s_mov_b64 vcc, s[50:51]
	v_cndmask_b32_sdwa v117, v1, v154, vcc dst_sel:WORD_1 dst_unused:UNUSED_PRESERVE src0_sel:WORD_1 src1_sel:WORD_1
	v_mfma_f32_32x32x16_f16 a[176:191], v[38:41], v[106:109], a[176:191]
	v_cndmask_b32_e64 v110, v138, v156, s[4:5]
	s_mov_b64 vcc, s[6:7]
	v_cndmask_b32_sdwa v110, v138, v156, vcc dst_sel:WORD_1 dst_unused:UNUSED_PRESERVE src0_sel:WORD_1 src1_sel:WORD_1
	v_cndmask_b32_e64 v111, v138, v158, s[8:9]
	s_mov_b64 vcc, s[10:11]
	v_cndmask_b32_sdwa v111, v138, v158, vcc dst_sel:WORD_1 dst_unused:UNUSED_PRESERVE src0_sel:WORD_1 src1_sel:WORD_1
	v_mfma_f32_32x32x16_f16 a[112:127], v[18:21], v[98:101], a[112:127]
	v_cndmask_b32_e64 v112, v138, v160, s[12:13]
	s_mov_b64 vcc, s[14:15]
	v_cndmask_b32_sdwa v112, v138, v160, vcc dst_sel:WORD_1 dst_unused:UNUSED_PRESERVE src0_sel:WORD_1 src1_sel:WORD_1
	v_cndmask_b32_e64 v113, v138, v162, s[16:17]
	s_mov_b64 vcc, s[18:19]
	v_cndmask_b32_sdwa v113, v138, v162, vcc dst_sel:WORD_1 dst_unused:UNUSED_PRESERVE src0_sel:WORD_1 src1_sel:WORD_1
	v_mfma_f32_32x32x16_f16 a[160:175], v[38:41], v[98:101], a[160:175]
	v_pk_add_f16 v148, v115, v114
	v_pk_add_f16 v149, v116, v117
	v_mfma_f32_32x32x16_f16 a[128:143], v[18:21], v[94:97], a[128:143]
	v_pk_add_f16 v150, v111, v110
	v_pk_add_f16 v151, v112, v113
	v_mfma_f32_32x32x16_f16 a[144:159], v[38:41], v[94:97], a[144:159]
	v_pk_add_f16 v148, v148, v149
	v_pk_add_f16 v150, v150, v151
	v_mfma_f32_32x32x16_f16 a[80:95], v[18:21], v[86:89], a[80:95]
	v_fma_mix_f32 v134, v148, 1.0, v134 op_sel_hi:[1,0,0]
	v_fma_mix_f32 v135, v150, 1.0, v135 op_sel_hi:[1,0,0]
	v_mfma_f32_32x32x16_f16 a[96:111], v[38:41], v[86:89], a[96:111]
	v_fma_mix_f32 v134, v148, 1.0, v134 op_sel:[1,0,0] op_sel_hi:[1,0,0]
	v_fma_mix_f32 v135, v150, 1.0, v135 op_sel:[1,0,0] op_sel_hi:[1,0,0]
	s_waitcnt lgkmcnt(0)
	v_mfma_f32_32x32x16_f16 a[0:15], v[114:117], v[50:53], a[0:15]
	s_load_dwordx16 s[36:51], s[30:31], 0x140
	s_load_dwordx16 s[4:19], s[30:31], 0x8140
	ds_read_b128 v[46:49], v145 offset:96
	ds_read_b128 v[42:45], v145 offset:2144
	v_mfma_f32_32x32x16_f16 a[240:255], v[110:113], v[50:53], a[240:255]
	ds_read_b128 v[74:77], v146
	v_pk_mul_f16 v148, v90, v136
	v_pk_mul_f16 v149, v82, v137
	v_pk_mul_f16 v150, v91, v136
	v_pk_mul_f16 v151, v83, v137
	v_mfma_f32_32x32x16_f16 a[16:31], v[114:117], v[54:57], a[16:31]
	ds_read_b128 v[126:129], v146 offset:4096
	v_pk_mul_f16 v152, v92, v136
	v_pk_mul_f16 v153, v84, v137
	v_pk_mul_f16 v154, v93, v136
	v_pk_mul_f16 v155, v85, v137
	v_mfma_f32_32x32x16_f16 a[224:239], v[110:113], v[54:57], a[224:239]
	ds_read_b128 v[122:125], v146 offset:8192
	v_pk_mul_f16 v156, v90, v140
	v_pk_mul_f16 v157, v82, v139
	v_pk_mul_f16 v158, v91, v140
	v_pk_mul_f16 v159, v83, v139
	v_mfma_f32_32x32x16_f16 a[32:47], v[114:117], v[58:61], a[32:47]
	ds_read_b128 v[118:121], v146 offset:12288
	v_pk_mul_f16 v160, v92, v140
	v_pk_mul_f16 v161, v84, v139
	v_pk_mul_f16 v162, v93, v140
	v_pk_mul_f16 v163, v85, v139
	v_mfma_f32_32x32x16_f16 a[208:223], v[110:113], v[58:61], a[208:223]
	ds_read_b128 v[106:109], v146 offset:16384
	v_pk_max_f16 v148, v148, v149
	v_pk_max_f16 v150, v150, v151
	v_pk_max_f16 v152, v152, v153
	v_pk_max_f16 v154, v154, v155
	v_mfma_f32_32x32x16_f16 a[48:63], v[114:117], v[62:65], a[48:63]
	ds_read_b128 v[98:101], v146 offset:20480
	v_pk_max_f16 v156, v156, v157
	v_pk_max_f16 v158, v158, v159
	v_pk_max_f16 v160, v160, v161
	v_pk_max_f16 v162, v162, v163
	v_mfma_f32_32x32x16_f16 a[192:207], v[110:113], v[62:65], a[192:207]
	ds_read_b128 v[94:97], v146 offset:24576
	v_cndmask_b32_e64 v18, v1, v148, s[68:69]
	s_mov_b64 vcc, s[70:71]
	v_cndmask_b32_sdwa v18, v1, v148, vcc dst_sel:WORD_1 dst_unused:UNUSED_PRESERVE src0_sel:WORD_1 src1_sel:WORD_1
	v_cndmask_b32_e64 v19, v1, v150, s[72:73]
	s_mov_b64 vcc, s[74:75]
	v_cndmask_b32_sdwa v19, v1, v150, vcc dst_sel:WORD_1 dst_unused:UNUSED_PRESERVE src0_sel:WORD_1 src1_sel:WORD_1
	v_mfma_f32_32x32x16_f16 a[64:79], v[114:117], v[66:69], a[64:79]
	ds_read_b128 v[86:89], v146 offset:28672
	v_cndmask_b32_e64 v20, v1, v152, s[76:77]
	s_mov_b64 vcc, s[78:79]
	v_cndmask_b32_sdwa v20, v1, v152, vcc dst_sel:WORD_1 dst_unused:UNUSED_PRESERVE src0_sel:WORD_1 src1_sel:WORD_1
	v_cndmask_b32_e64 v21, v1, v154, s[80:81]
	s_mov_b64 vcc, s[82:83]
	v_cndmask_b32_sdwa v21, v1, v154, vcc dst_sel:WORD_1 dst_unused:UNUSED_PRESERVE src0_sel:WORD_1 src1_sel:WORD_1
	v_mfma_f32_32x32x16_f16 a[176:191], v[110:113], v[66:69], a[176:191]
	v_cndmask_b32_e64 v38, v138, v156, s[52:53]
	s_mov_b64 vcc, s[54:55]
	v_cndmask_b32_sdwa v38, v138, v156, vcc dst_sel:WORD_1 dst_unused:UNUSED_PRESERVE src0_sel:WORD_1 src1_sel:WORD_1
	v_cndmask_b32_e64 v39, v138, v158, s[56:57]
	s_mov_b64 vcc, s[58:59]
	v_cndmask_b32_sdwa v39, v138, v158, vcc dst_sel:WORD_1 dst_unused:UNUSED_PRESERVE src0_sel:WORD_1 src1_sel:WORD_1
	v_mfma_f32_32x32x16_f16 a[112:127], v[114:117], v[70:73], a[112:127]
	v_cndmask_b32_e64 v40, v138, v160, s[60:61]
	s_mov_b64 vcc, s[62:63]
	v_cndmask_b32_sdwa v40, v138, v160, vcc dst_sel:WORD_1 dst_unused:UNUSED_PRESERVE src0_sel:WORD_1 src1_sel:WORD_1
	v_cndmask_b32_e64 v41, v138, v162, s[64:65]
	s_mov_b64 vcc, s[66:67]
	v_cndmask_b32_sdwa v41, v138, v162, vcc dst_sel:WORD_1 dst_unused:UNUSED_PRESERVE src0_sel:WORD_1 src1_sel:WORD_1
	v_mfma_f32_32x32x16_f16 a[160:175], v[110:113], v[70:73], a[160:175]
	v_pk_add_f16 v148, v19, v18
	v_pk_add_f16 v149, v20, v21
	v_mfma_f32_32x32x16_f16 a[128:143], v[114:117], v[78:81], a[128:143]
	v_pk_add_f16 v150, v39, v38
	v_pk_add_f16 v151, v40, v41
	v_mfma_f32_32x32x16_f16 a[144:159], v[110:113], v[78:81], a[144:159]
	v_pk_add_f16 v148, v148, v149
	v_pk_add_f16 v150, v150, v151
	v_mfma_f32_32x32x16_f16 a[80:95], v[114:117], v[102:105], a[80:95]
	v_fma_mix_f32 v134, v148, 1.0, v134 op_sel_hi:[1,0,0]
	v_fma_mix_f32 v135, v150, 1.0, v135 op_sel_hi:[1,0,0]
	v_mfma_f32_32x32x16_f16 a[96:111], v[110:113], v[102:105], a[96:111]
	v_fma_mix_f32 v134, v148, 1.0, v134 op_sel:[1,0,0] op_sel_hi:[1,0,0]
	v_fma_mix_f32 v135, v150, 1.0, v135 op_sel:[1,0,0] op_sel_hi:[1,0,0]
	s_add_i32 s92, s92, 0x9000
	s_cmp_lg_u32 s91, 2
	s_cselect_b32 s30, s92, 0
	s_add_u32 s20, s20, 0x100
	s_addc_u32 s21, s21, 0
	s_add_u32 s94, s94, 0x8000
	s_addc_u32 s95, s95, 0
	v_add_u32_e32 v145, 0x80, v145
	s_cmpk_eq_i32 s20, 0xf00
	s_mov_b32 s30, s91
	s_waitcnt vmcnt(0)
	s_waitcnt lgkmcnt(0)
	s_barrier
	s_cbranch_scc0 .LBB1_3
	s_waitcnt lgkmcnt(0)
	v_mfma_f32_32x32x16_f16 a[0:15], v[18:21], v[74:77], a[0:15]
	s_load_dwordx16 s[68:83], s[0:1], 0xf80
	s_load_dwordx16 s[52:67], s[0:1], 0x8f80
	ds_read_b128 v[90:93], v142 offset:1984
	ds_read_b128 v[82:85], v142 offset:4032
	v_mfma_f32_32x32x16_f16 a[240:255], v[38:41], v[74:77], a[240:255]
	ds_read_b128 v[50:53], v208
	v_pk_mul_f16 v148, v46, v136
	v_pk_mul_f16 v149, v42, v137
	v_pk_mul_f16 v150, v47, v136
	v_pk_mul_f16 v151, v43, v137
	v_mfma_f32_32x32x16_f16 a[16:31], v[18:21], v[126:129], a[16:31]
	ds_read_b128 v[54:57], v208 offset:4096
	v_pk_mul_f16 v152, v48, v136
	v_pk_mul_f16 v153, v44, v137
	v_pk_mul_f16 v154, v49, v136
	v_pk_mul_f16 v155, v45, v137
	v_mfma_f32_32x32x16_f16 a[224:239], v[38:41], v[126:129], a[224:239]
	ds_read_b128 v[58:61], v208 offset:8192
	v_pk_mul_f16 v156, v46, v140
	v_pk_mul_f16 v157, v42, v139
	v_pk_mul_f16 v158, v47, v140
	v_pk_mul_f16 v159, v43, v139
	v_mfma_f32_32x32x16_f16 a[32:47], v[18:21], v[122:125], a[32:47]
	ds_read_b128 v[62:65], v208 offset:12288
	v_pk_mul_f16 v160, v48, v140
	v_pk_mul_f16 v161, v44, v139
	v_pk_mul_f16 v162, v49, v140
	v_pk_mul_f16 v163, v45, v139
	v_mfma_f32_32x32x16_f16 a[208:223], v[38:41], v[122:125], a[208:223]
	ds_read_b128 v[66:69], v208 offset:16384
	v_pk_max_f16 v148, v148, v149
	v_pk_max_f16 v150, v150, v151
	v_pk_max_f16 v152, v152, v153
	v_pk_max_f16 v154, v154, v155
	v_mfma_f32_32x32x16_f16 a[48:63], v[18:21], v[118:121], a[48:63]
	ds_read_b128 v[70:73], v208 offset:20480
	v_pk_max_f16 v156, v156, v157
	v_pk_max_f16 v158, v158, v159
	v_pk_max_f16 v160, v160, v161
	v_pk_max_f16 v162, v162, v163
	v_mfma_f32_32x32x16_f16 a[192:207], v[38:41], v[118:121], a[192:207]
	ds_read_b128 v[78:81], v208 offset:24576
	v_cndmask_b32_e64 v114, v1, v148, s[36:37]
	s_mov_b64 vcc, s[38:39]
	v_cndmask_b32_sdwa v114, v1, v148, vcc dst_sel:WORD_1 dst_unused:UNUSED_PRESERVE src0_sel:WORD_1 src1_sel:WORD_1
	v_cndmask_b32_e64 v115, v1, v150, s[40:41]
	s_mov_b64 vcc, s[42:43]
	v_cndmask_b32_sdwa v115, v1, v150, vcc dst_sel:WORD_1 dst_unused:UNUSED_PRESERVE src0_sel:WORD_1 src1_sel:WORD_1
	v_mfma_f32_32x32x16_f16 a[64:79], v[18:21], v[106:109], a[64:79]
	ds_read_b128 v[102:105], v208 offset:28672
	v_cndmask_b32_e64 v116, v1, v152, s[44:45]
	s_mov_b64 vcc, s[46:47]
	v_cndmask_b32_sdwa v116, v1, v152, vcc dst_sel:WORD_1 dst_unused:UNUSED_PRESERVE src0_sel:WORD_1 src1_sel:WORD_1
	v_cndmask_b32_e64 v117, v1, v154, s[48:49]
	s_mov_b64 vcc, s[50:51]
	v_cndmask_b32_sdwa v117, v1, v154, vcc dst_sel:WORD_1 dst_unused:UNUSED_PRESERVE src0_sel:WORD_1 src1_sel:WORD_1
	v_mfma_f32_32x32x16_f16 a[176:191], v[38:41], v[106:109], a[176:191]
	v_cndmask_b32_e64 v110, v138, v156, s[4:5]
	s_mov_b64 vcc, s[6:7]
	v_cndmask_b32_sdwa v110, v138, v156, vcc dst_sel:WORD_1 dst_unused:UNUSED_PRESERVE src0_sel:WORD_1 src1_sel:WORD_1
	v_cndmask_b32_e64 v111, v138, v158, s[8:9]
	s_mov_b64 vcc, s[10:11]
	v_cndmask_b32_sdwa v111, v138, v158, vcc dst_sel:WORD_1 dst_unused:UNUSED_PRESERVE src0_sel:WORD_1 src1_sel:WORD_1
	v_mfma_f32_32x32x16_f16 a[112:127], v[18:21], v[98:101], a[112:127]
	v_cndmask_b32_e64 v112, v138, v160, s[12:13]
	s_mov_b64 vcc, s[14:15]
	v_cndmask_b32_sdwa v112, v138, v160, vcc dst_sel:WORD_1 dst_unused:UNUSED_PRESERVE src0_sel:WORD_1 src1_sel:WORD_1
	v_cndmask_b32_e64 v113, v138, v162, s[16:17]
	s_mov_b64 vcc, s[18:19]
	v_cndmask_b32_sdwa v113, v138, v162, vcc dst_sel:WORD_1 dst_unused:UNUSED_PRESERVE src0_sel:WORD_1 src1_sel:WORD_1
	v_mfma_f32_32x32x16_f16 a[160:175], v[38:41], v[98:101], a[160:175]
	v_pk_add_f16 v148, v115, v114
	v_pk_add_f16 v149, v116, v117
	v_mfma_f32_32x32x16_f16 a[128:143], v[18:21], v[94:97], a[128:143]
	v_pk_add_f16 v150, v111, v110
	v_pk_add_f16 v151, v112, v113
	v_mfma_f32_32x32x16_f16 a[144:159], v[38:41], v[94:97], a[144:159]
	v_pk_add_f16 v148, v148, v149
	v_pk_add_f16 v150, v150, v151
	v_mfma_f32_32x32x16_f16 a[80:95], v[18:21], v[86:89], a[80:95]
	v_fma_mix_f32 v134, v148, 1.0, v134 op_sel_hi:[1,0,0]
	v_fma_mix_f32 v135, v150, 1.0, v135 op_sel_hi:[1,0,0]
	v_mfma_f32_32x32x16_f16 a[96:111], v[38:41], v[86:89], a[96:111]
	v_fma_mix_f32 v134, v148, 1.0, v134 op_sel:[1,0,0] op_sel_hi:[1,0,0]
	v_fma_mix_f32 v135, v150, 1.0, v135 op_sel:[1,0,0] op_sel_hi:[1,0,0]
	s_waitcnt lgkmcnt(0)
	v_mfma_f32_32x32x16_f16 a[0:15], v[114:117], v[50:53], a[0:15]
	s_load_dwordx16 s[36:51], s[0:1], 0xfc0
	s_load_dwordx16 s[4:19], s[0:1], 0x8fc0
	ds_read_b128 v[46:49], v142 offset:2016
	ds_read_b128 v[42:45], v142 offset:4064
	v_mfma_f32_32x32x16_f16 a[240:255], v[110:113], v[50:53], a[240:255]
	ds_read_b128 v[74:77], v209
	v_pk_mul_f16 v148, v90, v136
	v_pk_mul_f16 v149, v82, v137
	v_pk_mul_f16 v150, v91, v136
	v_pk_mul_f16 v151, v83, v137
	v_mfma_f32_32x32x16_f16 a[16:31], v[114:117], v[54:57], a[16:31]
	ds_read_b128 v[126:129], v209 offset:4096
	v_pk_mul_f16 v152, v92, v136
	v_pk_mul_f16 v153, v84, v137
	v_pk_mul_f16 v154, v93, v136
	v_pk_mul_f16 v155, v85, v137
	v_mfma_f32_32x32x16_f16 a[224:239], v[110:113], v[54:57], a[224:239]
	ds_read_b128 v[122:125], v209 offset:8192
	v_pk_mul_f16 v156, v90, v140
	v_pk_mul_f16 v157, v82, v139
	v_pk_mul_f16 v158, v91, v140
	v_pk_mul_f16 v159, v83, v139
	v_mfma_f32_32x32x16_f16 a[32:47], v[114:117], v[58:61], a[32:47]
	ds_read_b128 v[118:121], v209 offset:12288
	v_pk_mul_f16 v160, v92, v140
	v_pk_mul_f16 v161, v84, v139
	v_pk_mul_f16 v162, v93, v140
	v_pk_mul_f16 v163, v85, v139
	v_mfma_f32_32x32x16_f16 a[208:223], v[110:113], v[58:61], a[208:223]
	ds_read_b128 v[106:109], v209 offset:16384
	v_pk_max_f16 v148, v148, v149
	v_pk_max_f16 v150, v150, v151
	v_pk_max_f16 v152, v152, v153
	v_pk_max_f16 v154, v154, v155
	v_mfma_f32_32x32x16_f16 a[48:63], v[114:117], v[62:65], a[48:63]
	ds_read_b128 v[98:101], v209 offset:20480
	v_pk_max_f16 v156, v156, v157
	v_pk_max_f16 v158, v158, v159
	v_pk_max_f16 v160, v160, v161
	v_pk_max_f16 v162, v162, v163
	v_mfma_f32_32x32x16_f16 a[192:207], v[110:113], v[62:65], a[192:207]
	ds_read_b128 v[94:97], v209 offset:24576
	v_cndmask_b32_e64 v18, v1, v148, s[68:69]
	s_mov_b64 vcc, s[70:71]
	v_cndmask_b32_sdwa v18, v1, v148, vcc dst_sel:WORD_1 dst_unused:UNUSED_PRESERVE src0_sel:WORD_1 src1_sel:WORD_1
	v_cndmask_b32_e64 v19, v1, v150, s[72:73]
	s_mov_b64 vcc, s[74:75]
	v_cndmask_b32_sdwa v19, v1, v150, vcc dst_sel:WORD_1 dst_unused:UNUSED_PRESERVE src0_sel:WORD_1 src1_sel:WORD_1
	v_mfma_f32_32x32x16_f16 a[64:79], v[114:117], v[66:69], a[64:79]
	ds_read_b128 v[86:89], v209 offset:28672
	v_cndmask_b32_e64 v20, v1, v152, s[76:77]
	s_mov_b64 vcc, s[78:79]
	v_cndmask_b32_sdwa v20, v1, v152, vcc dst_sel:WORD_1 dst_unused:UNUSED_PRESERVE src0_sel:WORD_1 src1_sel:WORD_1
	v_cndmask_b32_e64 v21, v1, v154, s[80:81]
	s_mov_b64 vcc, s[82:83]
	v_cndmask_b32_sdwa v21, v1, v154, vcc dst_sel:WORD_1 dst_unused:UNUSED_PRESERVE src0_sel:WORD_1 src1_sel:WORD_1
	v_mfma_f32_32x32x16_f16 a[176:191], v[110:113], v[66:69], a[176:191]
	v_cndmask_b32_e64 v38, v138, v156, s[52:53]
	s_mov_b64 vcc, s[54:55]
	v_cndmask_b32_sdwa v38, v138, v156, vcc dst_sel:WORD_1 dst_unused:UNUSED_PRESERVE src0_sel:WORD_1 src1_sel:WORD_1
	v_cndmask_b32_e64 v39, v138, v158, s[56:57]
	s_mov_b64 vcc, s[58:59]
	v_cndmask_b32_sdwa v39, v138, v158, vcc dst_sel:WORD_1 dst_unused:UNUSED_PRESERVE src0_sel:WORD_1 src1_sel:WORD_1
	v_mfma_f32_32x32x16_f16 a[112:127], v[114:117], v[70:73], a[112:127]
	v_cndmask_b32_e64 v40, v138, v160, s[60:61]
	s_mov_b64 vcc, s[62:63]
	v_cndmask_b32_sdwa v40, v138, v160, vcc dst_sel:WORD_1 dst_unused:UNUSED_PRESERVE src0_sel:WORD_1 src1_sel:WORD_1
	v_cndmask_b32_e64 v41, v138, v162, s[64:65]
	s_mov_b64 vcc, s[66:67]
	v_cndmask_b32_sdwa v41, v138, v162, vcc dst_sel:WORD_1 dst_unused:UNUSED_PRESERVE src0_sel:WORD_1 src1_sel:WORD_1
	v_mfma_f32_32x32x16_f16 a[160:175], v[110:113], v[70:73], a[160:175]
	v_pk_add_f16 v148, v19, v18
	v_pk_add_f16 v149, v20, v21
	v_mfma_f32_32x32x16_f16 a[128:143], v[114:117], v[78:81], a[128:143]
	v_pk_add_f16 v150, v39, v38
	v_pk_add_f16 v151, v40, v41
	v_mfma_f32_32x32x16_f16 a[144:159], v[110:113], v[78:81], a[144:159]
	v_pk_add_f16 v148, v148, v149
	v_pk_add_f16 v150, v150, v151
	v_mfma_f32_32x32x16_f16 a[80:95], v[114:117], v[102:105], a[80:95]
	v_fma_mix_f32 v134, v148, 1.0, v134 op_sel_hi:[1,0,0]
	v_fma_mix_f32 v135, v150, 1.0, v135 op_sel_hi:[1,0,0]
	v_mfma_f32_32x32x16_f16 a[96:111], v[110:113], v[102:105], a[96:111]
	v_fma_mix_f32 v134, v148, 1.0, v134 op_sel:[1,0,0] op_sel_hi:[1,0,0]
	v_fma_mix_f32 v135, v150, 1.0, v135 op_sel:[1,0,0] op_sel_hi:[1,0,0]
	s_waitcnt lgkmcnt(0)
	v_mfma_f32_32x32x16_f16 a[0:15], v[18:21], v[74:77], a[0:15]
	v_mfma_f32_32x32x16_f16 a[240:255], v[38:41], v[74:77], a[240:255]
	ds_read_b128 v[50:53], v210
	v_pk_mul_f16 v148, v46, v136
	v_pk_mul_f16 v149, v42, v137
	v_pk_mul_f16 v150, v47, v136
	v_pk_mul_f16 v151, v43, v137
	v_mfma_f32_32x32x16_f16 a[16:31], v[18:21], v[126:129], a[16:31]
	ds_read_b128 v[54:57], v210 offset:4096
	v_pk_mul_f16 v152, v48, v136
	v_pk_mul_f16 v153, v44, v137
	v_pk_mul_f16 v154, v49, v136
	v_pk_mul_f16 v155, v45, v137
	v_mfma_f32_32x32x16_f16 a[224:239], v[38:41], v[126:129], a[224:239]
	ds_read_b128 v[58:61], v210 offset:8192
	v_pk_mul_f16 v156, v46, v140
	v_pk_mul_f16 v157, v42, v139
	v_pk_mul_f16 v158, v47, v140
	v_pk_mul_f16 v159, v43, v139
	v_mfma_f32_32x32x16_f16 a[32:47], v[18:21], v[122:125], a[32:47]
	ds_read_b128 v[62:65], v210 offset:12288
	v_pk_mul_f16 v160, v48, v140
	v_pk_mul_f16 v161, v44, v139
	v_pk_mul_f16 v162, v49, v140
	v_pk_mul_f16 v163, v45, v139
	v_mfma_f32_32x32x16_f16 a[208:223], v[38:41], v[122:125], a[208:223]
	ds_read_b128 v[66:69], v210 offset:16384
	v_pk_max_f16 v148, v148, v149
	v_pk_max_f16 v150, v150, v151
	v_pk_max_f16 v152, v152, v153
	v_pk_max_f16 v154, v154, v155
	v_mfma_f32_32x32x16_f16 a[48:63], v[18:21], v[118:121], a[48:63]
	ds_read_b128 v[70:73], v210 offset:20480
	v_pk_max_f16 v156, v156, v157
	v_pk_max_f16 v158, v158, v159
	v_pk_max_f16 v160, v160, v161
	v_pk_max_f16 v162, v162, v163
	v_mfma_f32_32x32x16_f16 a[192:207], v[38:41], v[118:121], a[192:207]
	ds_read_b128 v[78:81], v210 offset:24576
	v_cndmask_b32_e64 v114, v1, v148, s[36:37]
	s_mov_b64 vcc, s[38:39]
	v_cndmask_b32_sdwa v114, v1, v148, vcc dst_sel:WORD_1 dst_unused:UNUSED_PRESERVE src0_sel:WORD_1 src1_sel:WORD_1
	v_cndmask_b32_e64 v115, v1, v150, s[40:41]
	s_mov_b64 vcc, s[42:43]
	v_cndmask_b32_sdwa v115, v1, v150, vcc dst_sel:WORD_1 dst_unused:UNUSED_PRESERVE src0_sel:WORD_1 src1_sel:WORD_1
	v_mfma_f32_32x32x16_f16 a[64:79], v[18:21], v[106:109], a[64:79]
	ds_read_b128 v[102:105], v210 offset:28672
	v_cndmask_b32_e64 v116, v1, v152, s[44:45]
	s_mov_b64 vcc, s[46:47]
	v_cndmask_b32_sdwa v116, v1, v152, vcc dst_sel:WORD_1 dst_unused:UNUSED_PRESERVE src0_sel:WORD_1 src1_sel:WORD_1
	v_cndmask_b32_e64 v117, v1, v154, s[48:49]
	s_mov_b64 vcc, s[50:51]
	v_cndmask_b32_sdwa v117, v1, v154, vcc dst_sel:WORD_1 dst_unused:UNUSED_PRESERVE src0_sel:WORD_1 src1_sel:WORD_1
	v_mfma_f32_32x32x16_f16 a[176:191], v[38:41], v[106:109], a[176:191]
	v_cndmask_b32_e64 v110, v138, v156, s[4:5]
	s_mov_b64 vcc, s[6:7]
	v_cndmask_b32_sdwa v110, v138, v156, vcc dst_sel:WORD_1 dst_unused:UNUSED_PRESERVE src0_sel:WORD_1 src1_sel:WORD_1
	v_cndmask_b32_e64 v111, v138, v158, s[8:9]
	s_mov_b64 vcc, s[10:11]
	v_cndmask_b32_sdwa v111, v138, v158, vcc dst_sel:WORD_1 dst_unused:UNUSED_PRESERVE src0_sel:WORD_1 src1_sel:WORD_1
	v_mfma_f32_32x32x16_f16 a[112:127], v[18:21], v[98:101], a[112:127]
	v_cndmask_b32_e64 v112, v138, v160, s[12:13]
	s_mov_b64 vcc, s[14:15]
	v_cndmask_b32_sdwa v112, v138, v160, vcc dst_sel:WORD_1 dst_unused:UNUSED_PRESERVE src0_sel:WORD_1 src1_sel:WORD_1
	v_cndmask_b32_e64 v113, v138, v162, s[16:17]
	s_mov_b64 vcc, s[18:19]
	v_cndmask_b32_sdwa v113, v138, v162, vcc dst_sel:WORD_1 dst_unused:UNUSED_PRESERVE src0_sel:WORD_1 src1_sel:WORD_1
	v_mfma_f32_32x32x16_f16 a[160:175], v[38:41], v[98:101], a[160:175]
	v_pk_add_f16 v148, v115, v114
	v_pk_add_f16 v149, v116, v117
	v_mfma_f32_32x32x16_f16 a[128:143], v[18:21], v[94:97], a[128:143]
	v_pk_add_f16 v150, v111, v110
	v_pk_add_f16 v151, v112, v113
	v_mfma_f32_32x32x16_f16 a[144:159], v[38:41], v[94:97], a[144:159]
	v_pk_add_f16 v148, v148, v149
	v_pk_add_f16 v150, v150, v151
	v_mfma_f32_32x32x16_f16 a[80:95], v[18:21], v[86:89], a[80:95]
	v_fma_mix_f32 v134, v148, 1.0, v134 op_sel_hi:[1,0,0]
	v_fma_mix_f32 v135, v150, 1.0, v135 op_sel_hi:[1,0,0]
	v_mfma_f32_32x32x16_f16 a[96:111], v[38:41], v[86:89], a[96:111]
	v_fma_mix_f32 v134, v148, 1.0, v134 op_sel:[1,0,0] op_sel_hi:[1,0,0]
	v_fma_mix_f32 v135, v150, 1.0, v135 op_sel:[1,0,0] op_sel_hi:[1,0,0]
	s_waitcnt lgkmcnt(0)
	v_mfma_f32_32x32x16_f16 a[0:15], v[114:117], v[50:53], a[0:15]
	v_mfma_f32_32x32x16_f16 a[240:255], v[110:113], v[50:53], a[240:255]
	v_mfma_f32_32x32x16_f16 a[16:31], v[114:117], v[54:57], a[16:31]
	v_mfma_f32_32x32x16_f16 a[224:239], v[110:113], v[54:57], a[224:239]
	v_mfma_f32_32x32x16_f16 a[32:47], v[114:117], v[58:61], a[32:47]
	v_mfma_f32_32x32x16_f16 a[208:223], v[110:113], v[58:61], a[208:223]
	v_mfma_f32_32x32x16_f16 a[48:63], v[114:117], v[62:65], a[48:63]
	v_mfma_f32_32x32x16_f16 a[192:207], v[110:113], v[62:65], a[192:207]
	v_mfma_f32_32x32x16_f16 a[64:79], v[114:117], v[66:69], a[64:79]
	v_mfma_f32_32x32x16_f16 a[176:191], v[110:113], v[66:69], a[176:191]
	v_mfma_f32_32x32x16_f16 a[112:127], v[114:117], v[70:73], a[112:127]
	v_mfma_f32_32x32x16_f16 a[160:175], v[110:113], v[70:73], a[160:175]
	v_mfma_f32_32x32x16_f16 a[128:143], v[114:117], v[78:81], a[128:143]
	v_mfma_f32_32x32x16_f16 a[144:159], v[110:113], v[78:81], a[144:159]
	v_mfma_f32_32x32x16_f16 a[80:95], v[114:117], v[102:105], a[80:95]
	v_mfma_f32_32x32x16_f16 a[96:111], v[110:113], v[102:105], a[96:111]
	v_readfirstlane_b32 s1, v0
	s_and_b32 s0, s3, 0xffffff00
	s_andn2_b32 s1, s1, 63
	s_add_i32 s4, s1, s0
	s_lshl_b32 s0, s2, 13
	s_and_b32 s6, s0, 0xe000
	s_ashr_i32 s5, s4, 31
	s_add_u32 s0, s4, s6
	s_addc_u32 s1, s5, 0
	s_lshl_b64 s[2:3], s[0:1], 9
	v_lshrrev_b32_e32 v0, 3, v132
	s_add_u32 s2, s22, s2
	v_and_b32_e32 v3, 12, v0
	s_addc_u32 s3, s23, s3
	v_lshlrev_b32_e32 v0, 9, v3
	v_mov_b32_e32 v1, 0
	v_lshl_add_u64 v[4:5], s[2:3], 0, v[0:1]
	v_lshlrev_b32_e32 v0, 4, v132
	v_and_b32_e32 v0, 0x1f0, v0
	v_lshl_add_u64 v[4:5], v[4:5], 0, v[0:1]
	v_accvgpr_read_b32 v6, a0
	v_accvgpr_read_b32 v7, a16
	v_accvgpr_read_b32 v8, a32
	v_max3_f32 v0, |v6|, |v7|, |v8|
	v_accvgpr_read_b32 v9, a48
	v_accvgpr_read_b32 v14, a64
	v_max3_f32 v0, |v0|, |v9|, |v14|
	v_accvgpr_read_b32 v15, a112
	v_accvgpr_read_b32 v16, a128
	v_max3_f32 v0, |v0|, |v15|, |v16|
	v_accvgpr_read_b32 v17, a80
	v_max3_f32 v10, |v0|, |v17|, |v17|
	v_accvgpr_read_b32 v18, a1
	v_accvgpr_read_b32 v19, a17
	v_accvgpr_read_b32 v20, a33
	v_max3_f32 v0, |v18|, |v19|, |v20|
	v_accvgpr_read_b32 v21, a49
	v_accvgpr_read_b32 v22, a65
	v_max3_f32 v0, |v0|, |v21|, |v22|
	v_accvgpr_read_b32 v23, a113
	v_accvgpr_read_b32 v24, a129
	v_max3_f32 v0, |v0|, |v23|, |v24|
	v_accvgpr_read_b32 v25, a81
	v_max3_f32 v11, |v0|, |v25|, |v25|
	v_accvgpr_read_b32 v26, a2
	v_accvgpr_read_b32 v27, a18
	v_accvgpr_read_b32 v28, a34
	v_max3_f32 v0, |v26|, |v27|, |v28|
	v_accvgpr_read_b32 v29, a50
	v_accvgpr_read_b32 v30, a66
	v_max3_f32 v0, |v0|, |v29|, |v30|
	v_accvgpr_read_b32 v31, a114
	v_accvgpr_read_b32 v32, a130
	v_max3_f32 v0, |v0|, |v31|, |v32|
	v_accvgpr_read_b32 v33, a82
	v_max3_f32 v12, |v0|, |v33|, |v33|
	v_accvgpr_read_b32 v34, a3
	v_accvgpr_read_b32 v35, a19
	v_accvgpr_read_b32 v36, a35
	v_max3_f32 v0, |v34|, |v35|, |v36|
	v_accvgpr_read_b32 v37, a51
	v_accvgpr_read_b32 v38, a67
	v_max3_f32 v0, |v0|, |v37|, |v38|
	v_accvgpr_read_b32 v39, a115
	v_accvgpr_read_b32 v40, a131
	v_max3_f32 v0, |v0|, |v39|, |v40|
	v_accvgpr_read_b32 v41, a83
	v_max3_f32 v13, |v0|, |v41|, |v41|
	v_lshlrev_b32_e32 v0, 2, v3
	s_nop 1
	v_max_f32_dpp v10, v10, v10 quad_perm:[1,0,3,2] row_mask:0xf bank_mask:0xf
	v_max_f32_dpp v11, v11, v11 quad_perm:[1,0,3,2] row_mask:0xf bank_mask:0xf
	v_max_f32_dpp v12, v12, v12 quad_perm:[1,0,3,2] row_mask:0xf bank_mask:0xf
	v_max_f32_dpp v13, v13, v13 quad_perm:[1,0,3,2] row_mask:0xf bank_mask:0xf
	v_max_f32_dpp v10, v10, v10 quad_perm:[2,3,0,1] row_mask:0xf bank_mask:0xf
	v_max_f32_dpp v11, v11, v11 quad_perm:[2,3,0,1] row_mask:0xf bank_mask:0xf
	v_max_f32_dpp v12, v12, v12 quad_perm:[2,3,0,1] row_mask:0xf bank_mask:0xf
	v_max_f32_dpp v13, v13, v13 quad_perm:[2,3,0,1] row_mask:0xf bank_mask:0xf
	v_max_f32_dpp v10, v10, v10 row_half_mirror row_mask:0xf bank_mask:0xf
	v_max_f32_dpp v11, v11, v11 row_half_mirror row_mask:0xf bank_mask:0xf
	v_max_f32_dpp v12, v12, v12 row_half_mirror row_mask:0xf bank_mask:0xf
	v_max_f32_dpp v13, v13, v13 row_half_mirror row_mask:0xf bank_mask:0xf
	v_max_f32_dpp v10, v10, v10 row_mirror row_mask:0xf bank_mask:0xf
	v_max_f32_dpp v11, v11, v11 row_mirror row_mask:0xf bank_mask:0xf
	v_max_f32_dpp v12, v12, v12 row_mirror row_mask:0xf bank_mask:0xf
	v_max_f32_dpp v13, v13, v13 row_mirror row_mask:0xf bank_mask:0xf
	s_nop 0
	ds_swizzle_b32 v232, v10 offset:swizzle(SWAP,16)
	ds_swizzle_b32 v233, v12 offset:swizzle(SWAP,16)
	ds_swizzle_b32 v234, v11 offset:swizzle(SWAP,16)
	ds_swizzle_b32 v235, v13 offset:swizzle(SWAP,16)
	s_waitcnt lgkmcnt(0)
	v_max_f32_e32 v10, v10, v232
	v_rcp_f32_e32 v42, v10
	v_cmp_lt_f32_e32 vcc, 0, v10
	s_waitcnt lgkmcnt(0)
	v_max_f32_e32 v12, v12, v233
	s_waitcnt lgkmcnt(0)
	v_max_f32_e32 v11, v11, v234
	s_lshl_b32 s2, s6, 2
	v_cndmask_b32_e32 v3, 0, v42, vcc
	v_pk_mul_f32 v[224:225], v[6:7], v[2:3] op_sel:[0,1] op_sel_hi:[1,1]
	v_pk_mul_f32 v[226:227], v[8:9], v[2:3] op_sel:[0,1] op_sel_hi:[1,1]
	v_cvt_pknorm_i16_f32 v6, v224, v225
	v_cvt_pknorm_i16_f32 v7, v226, v227
	v_pk_mul_f32 v[228:229], v[14:15], v[2:3] op_sel:[0,1] op_sel_hi:[1,1]
	v_rcp_f32_e32 v14, v11
	v_cvt_pknorm_i16_f32 v8, v228, v229
	v_pk_mul_f32 v[230:231], v[16:17], v[2:3] op_sel:[0,1] op_sel_hi:[1,1]
	v_cmp_lt_f32_e32 vcc, 0, v11
	v_cvt_pknorm_i16_f32 v9, v230, v231
	global_store_dwordx4 v[4:5], v[6:9], off sc0 sc1
	s_add_u32 s6, s24, s2
	v_cndmask_b32_e32 v3, 0, v14, vcc
	v_pk_mul_f32 v[224:225], v[18:19], v[2:3] op_sel:[0,1] op_sel_hi:[1,1]
	v_pk_mul_f32 v[226:227], v[20:21], v[2:3] op_sel:[0,1] op_sel_hi:[1,1]
	v_cvt_pknorm_i16_f32 v6, v224, v225
	v_cvt_pknorm_i16_f32 v7, v226, v227
	v_pk_mul_f32 v[228:229], v[22:23], v[2:3] op_sel:[0,1] op_sel_hi:[1,1]
	v_pk_mul_f32 v[230:231], v[24:25], v[2:3] op_sel:[0,1] op_sel_hi:[1,1]
	v_cvt_pknorm_i16_f32 v8, v228, v229
	v_cvt_pknorm_i16_f32 v9, v230, v231
	v_rcp_f32_e32 v3, v12
	s_addc_u32 s7, s25, 0
	s_lshl_b64 s[2:3], s[4:5], 2
	s_mov_b64 s[4:5], 0x200
	s_add_u32 s2, s6, s2
	v_lshl_add_u64 v[14:15], v[4:5], 0, s[4:5]
	s_mov_b32 s4, 0x38000100
	v_cmp_lt_f32_e32 vcc, 0, v12
	s_addc_u32 s3, s7, s3
	global_store_dwordx4 v[14:15], v[6:9], off sc0 sc1
	s_nop 1
	v_pk_mul_f32 v[6:7], v[10:11], s[4:5] op_sel_hi:[1,0]
	v_cndmask_b32_e32 v3, 0, v3, vcc
	global_store_dwordx2 v0, v[6:7], s[2:3]
	v_pk_mul_f32 v[224:225], v[26:27], v[2:3] op_sel:[0,1] op_sel_hi:[1,1]
	v_pk_mul_f32 v[226:227], v[28:29], v[2:3] op_sel:[0,1] op_sel_hi:[1,1]
	v_cvt_pknorm_i16_f32 v6, v224, v225
	v_cvt_pknorm_i16_f32 v7, v226, v227
	v_pk_mul_f32 v[228:229], v[30:31], v[2:3] op_sel:[0,1] op_sel_hi:[1,1]
	v_pk_mul_f32 v[230:231], v[32:33], v[2:3] op_sel:[0,1] op_sel_hi:[1,1]
	v_cvt_pknorm_i16_f32 v8, v228, v229
	s_waitcnt lgkmcnt(0)
	v_max_f32_e32 v13, v13, v235
	v_cvt_pknorm_i16_f32 v9, v230, v231
	v_rcp_f32_e32 v3, v13
	v_cmp_lt_f32_e32 vcc, 0, v13
	s_mov_b64 s[6:7], 0x400
	v_lshl_add_u64 v[10:11], v[4:5], 0, s[6:7]
	v_cndmask_b32_e32 v3, 0, v3, vcc
	global_store_dwordx4 v[10:11], v[6:9], off sc0 sc1
	v_pk_mul_f32 v[224:225], v[34:35], v[2:3] op_sel:[0,1] op_sel_hi:[1,1]
	v_pk_mul_f32 v[226:227], v[36:37], v[2:3] op_sel:[0,1] op_sel_hi:[1,1]
	v_cvt_pknorm_i16_f32 v6, v224, v225
	v_cvt_pknorm_i16_f32 v7, v226, v227
	v_pk_mul_f32 v[228:229], v[38:39], v[2:3] op_sel:[0,1] op_sel_hi:[1,1]
	v_pk_mul_f32 v[230:231], v[40:41], v[2:3] op_sel:[0,1] op_sel_hi:[1,1]
	v_cvt_pknorm_i16_f32 v8, v228, v229
	s_mov_b64 s[6:7], 0x600
	v_cvt_pknorm_i16_f32 v9, v230, v231
	v_lshl_add_u64 v[10:11], v[4:5], 0, s[6:7]
	global_store_dwordx4 v[10:11], v[6:9], off sc0 sc1
	s_nop 1
	v_pk_mul_f32 v[6:7], v[12:13], s[4:5] op_sel_hi:[1,0]
	v_lshlrev_b32_e32 v2, 2, v132
	global_store_dwordx2 v0, v[6:7], s[2:3] offset:8
	v_accvgpr_read_b32 v42, a4
	v_accvgpr_read_b32 v6, a20
	v_accvgpr_read_b32 v7, a36
	v_max3_f32 v8, |v42|, |v6|, |v7|
	v_accvgpr_read_b32 v9, a52
	v_accvgpr_read_b32 v14, a68
	v_max3_f32 v8, |v8|, |v9|, |v14|
	v_accvgpr_read_b32 v15, a116
	v_accvgpr_read_b32 v16, a132
	v_max3_f32 v8, |v8|, |v15|, |v16|
	v_accvgpr_read_b32 v10, a84
	v_accvgpr_read_b32 v43, a5
	v_accvgpr_read_b32 v17, a84
	v_max3_f32 v8, |v8|, |v17|, |v10|
	v_accvgpr_read_b32 v19, a21
	v_accvgpr_read_b32 v20, a37
	v_max3_f32 v10, |v43|, |v19|, |v20|
	v_accvgpr_read_b32 v21, a53
	v_accvgpr_read_b32 v22, a69
	v_max3_f32 v10, |v10|, |v21|, |v22|
	v_accvgpr_read_b32 v23, a117
	v_accvgpr_read_b32 v24, a133
	v_max3_f32 v10, |v10|, |v23|, |v24|
	v_accvgpr_read_b32 v44, a6
	v_accvgpr_read_b32 v25, a85
	v_max3_f32 v11, |v10|, |v25|, |v25|
	v_accvgpr_read_b32 v27, a22
	v_accvgpr_read_b32 v28, a38
	v_max3_f32 v10, |v44|, |v27|, |v28|
	v_accvgpr_read_b32 v29, a54
	v_accvgpr_read_b32 v30, a70
	v_max3_f32 v10, |v10|, |v29|, |v30|
	v_accvgpr_read_b32 v31, a118
	v_accvgpr_read_b32 v32, a134
	v_max3_f32 v10, |v10|, |v31|, |v32|
	v_accvgpr_read_b32 v45, a7
	v_accvgpr_read_b32 v33, a86
	v_max3_f32 v12, |v10|, |v33|, |v33|
	v_accvgpr_read_b32 v35, a23
	v_accvgpr_read_b32 v36, a39
	v_max3_f32 v10, |v45|, |v35|, |v36|
	v_accvgpr_read_b32 v37, a55
	v_accvgpr_read_b32 v38, a71
	v_max3_f32 v10, |v10|, |v37|, |v38|
	v_accvgpr_read_b32 v39, a119
	v_accvgpr_read_b32 v40, a135
	v_max3_f32 v10, |v10|, |v39|, |v40|
	v_accvgpr_read_b32 v41, a87
	v_max3_f32 v13, |v10|, |v41|, |v41|
	v_mov_b32_e32 v3, v42
	s_nop 1
	v_max_f32_dpp v8, v8, v8 quad_perm:[1,0,3,2] row_mask:0xf bank_mask:0xf
	v_max_f32_dpp v11, v11, v11 quad_perm:[1,0,3,2] row_mask:0xf bank_mask:0xf
	v_max_f32_dpp v12, v12, v12 quad_perm:[1,0,3,2] row_mask:0xf bank_mask:0xf
	v_max_f32_dpp v13, v13, v13 quad_perm:[1,0,3,2] row_mask:0xf bank_mask:0xf
	v_max_f32_dpp v8, v8, v8 quad_perm:[2,3,0,1] row_mask:0xf bank_mask:0xf
	v_max_f32_dpp v11, v11, v11 quad_perm:[2,3,0,1] row_mask:0xf bank_mask:0xf
	v_max_f32_dpp v12, v12, v12 quad_perm:[2,3,0,1] row_mask:0xf bank_mask:0xf
	v_max_f32_dpp v13, v13, v13 quad_perm:[2,3,0,1] row_mask:0xf bank_mask:0xf
	v_max_f32_dpp v8, v8, v8 row_half_mirror row_mask:0xf bank_mask:0xf
	v_max_f32_dpp v11, v11, v11 row_half_mirror row_mask:0xf bank_mask:0xf
	v_max_f32_dpp v12, v12, v12 row_half_mirror row_mask:0xf bank_mask:0xf
	v_max_f32_dpp v13, v13, v13 row_half_mirror row_mask:0xf bank_mask:0xf
	v_max_f32_dpp v8, v8, v8 row_mirror row_mask:0xf bank_mask:0xf
	v_max_f32_dpp v11, v11, v11 row_mirror row_mask:0xf bank_mask:0xf
	v_max_f32_dpp v12, v12, v12 row_mirror row_mask:0xf bank_mask:0xf
	v_max_f32_dpp v13, v13, v13 row_mirror row_mask:0xf bank_mask:0xf
	s_nop 0
	ds_swizzle_b32 v232, v8 offset:swizzle(SWAP,16)
	ds_swizzle_b32 v233, v11 offset:swizzle(SWAP,16)
	ds_swizzle_b32 v234, v12 offset:swizzle(SWAP,16)
	ds_swizzle_b32 v235, v13 offset:swizzle(SWAP,16)
	s_waitcnt lgkmcnt(0)
	v_max_f32_e32 v10, v8, v232
	v_rcp_f32_e32 v8, v10
	v_cmp_lt_f32_e32 vcc, 0, v10
	s_waitcnt lgkmcnt(0)
	v_max_f32_e32 v11, v11, v233
	v_mov_b32_e32 v18, v43
	s_mov_b64 s[6:7], 0x1000
	v_cndmask_b32_e32 v42, 0, v8, vcc
	v_mul_f32_e32 v3, v42, v3
	v_mul_f32_e32 v6, v42, v6
	v_cvt_pknorm_i16_f32 v6, v3, v6
	v_mul_f32_e32 v3, v42, v7
	v_mul_f32_e32 v7, v42, v9
	v_cvt_pknorm_i16_f32 v7, v3, v7
	v_pk_mul_f32 v[224:225], v[14:15], v[42:43] op_sel_hi:[1,0]
	v_pk_mul_f32 v[226:227], v[16:17], v[42:43] op_sel_hi:[1,0]
	v_cvt_pknorm_i16_f32 v8, v224, v225
	v_cvt_pknorm_i16_f32 v9, v226, v227
	v_rcp_f32_e32 v3, v11
	v_cmp_lt_f32_e32 vcc, 0, v11
	v_lshl_add_u64 v[14:15], v[4:5], 0, s[6:7]
	global_store_dwordx4 v[14:15], v[6:9], off sc0 sc1
	v_cndmask_b32_e32 v3, 0, v3, vcc
	v_pk_mul_f32 v[228:229], v[18:19], v[2:3] op_sel:[0,1] op_sel_hi:[1,1]
	v_pk_mul_f32 v[230:231], v[20:21], v[2:3] op_sel:[0,1] op_sel_hi:[1,1]
	v_cvt_pknorm_i16_f32 v6, v228, v229
	v_cvt_pknorm_i16_f32 v7, v230, v231
	v_pk_mul_f32 v[224:225], v[22:23], v[2:3] op_sel:[0,1] op_sel_hi:[1,1]
	v_pk_mul_f32 v[226:227], v[24:25], v[2:3] op_sel:[0,1] op_sel_hi:[1,1]
	v_cvt_pknorm_i16_f32 v8, v224, v225
	s_waitcnt lgkmcnt(0)
	v_max_f32_e32 v12, v12, v234
	v_cvt_pknorm_i16_f32 v9, v226, v227
	v_rcp_f32_e32 v3, v12
	s_mov_b64 s[6:7], 0x1200
	v_cmp_lt_f32_e32 vcc, 0, v12
	v_mov_b32_e32 v26, v44
	v_lshl_add_u64 v[14:15], v[4:5], 0, s[6:7]
	global_store_dwordx4 v[14:15], v[6:9], off sc0 sc1
	s_nop 1
	v_pk_mul_f32 v[6:7], v[10:11], s[4:5] op_sel_hi:[1,0]
	v_cndmask_b32_e32 v3, 0, v3, vcc
	global_store_dwordx2 v0, v[6:7], s[2:3] offset:32
	v_pk_mul_f32 v[228:229], v[26:27], v[2:3] op_sel:[0,1] op_sel_hi:[1,1]
	v_pk_mul_f32 v[230:231], v[28:29], v[2:3] op_sel:[0,1] op_sel_hi:[1,1]
	v_cvt_pknorm_i16_f32 v6, v228, v229
	v_cvt_pknorm_i16_f32 v7, v230, v231
	v_pk_mul_f32 v[224:225], v[30:31], v[2:3] op_sel:[0,1] op_sel_hi:[1,1]
	v_pk_mul_f32 v[226:227], v[32:33], v[2:3] op_sel:[0,1] op_sel_hi:[1,1]
	v_cvt_pknorm_i16_f32 v8, v224, v225
	s_waitcnt lgkmcnt(0)
	v_max_f32_e32 v13, v13, v235
	v_cvt_pknorm_i16_f32 v9, v226, v227
	v_rcp_f32_e32 v3, v13
	v_cmp_lt_f32_e32 vcc, 0, v13
	v_mov_b32_e32 v34, v45
	s_mov_b64 s[6:7], 0x1400
	v_cndmask_b32_e32 v3, 0, v3, vcc
	v_lshl_add_u64 v[10:11], v[4:5], 0, s[6:7]
	global_store_dwordx4 v[10:11], v[6:9], off sc0 sc1
	v_pk_mul_f32 v[228:229], v[34:35], v[2:3] op_sel:[0,1] op_sel_hi:[1,1]
	v_pk_mul_f32 v[230:231], v[36:37], v[2:3] op_sel:[0,1] op_sel_hi:[1,1]
	v_cvt_pknorm_i16_f32 v6, v228, v229
	v_cvt_pknorm_i16_f32 v7, v230, v231
	v_pk_mul_f32 v[224:225], v[38:39], v[2:3] op_sel:[0,1] op_sel_hi:[1,1]
	v_pk_mul_f32 v[226:227], v[40:41], v[2:3] op_sel:[0,1] op_sel_hi:[1,1]
	v_cvt_pknorm_i16_f32 v8, v224, v225
	s_mov_b64 s[6:7], 0x1600
	v_cvt_pknorm_i16_f32 v9, v226, v227
	v_lshl_add_u64 v[10:11], v[4:5], 0, s[6:7]
	global_store_dwordx4 v[10:11], v[6:9], off sc0 sc1
	s_nop 1
	v_pk_mul_f32 v[6:7], v[12:13], s[4:5] op_sel_hi:[1,0]
	v_accvgpr_read_b32 v46, a8
	v_accvgpr_read_b32 v47, a9
	v_accvgpr_read_b32 v48, a10
	v_accvgpr_read_b32 v49, a11
	v_accvgpr_read_b32 v50, a12
	v_accvgpr_read_b32 v51, a13
	v_accvgpr_read_b32 v52, a14
	v_accvgpr_read_b32 v53, a15
	global_store_dwordx2 v0, v[6:7], s[2:3] offset:40
	v_mov_b64_e32 v[42:43], v[46:47]
	v_accvgpr_read_b32 v6, a24
	v_accvgpr_read_b32 v7, a40
	v_max3_f32 v8, |v42|, |v6|, |v7|
	v_accvgpr_read_b32 v9, a56
	v_accvgpr_read_b32 v14, a72
	v_max3_f32 v8, |v8|, |v9|, |v14|
	v_accvgpr_read_b32 v15, a120
	v_accvgpr_read_b32 v16, a136
	v_max3_f32 v8, |v8|, |v15|, |v16|
	v_accvgpr_read_b32 v10, a88
	v_accvgpr_read_b32 v17, a88
	v_max3_f32 v8, |v8|, |v17|, |v10|
	v_accvgpr_read_b32 v19, a25
	v_accvgpr_read_b32 v20, a41
	v_max3_f32 v10, |v43|, |v19|, |v20|
	v_accvgpr_read_b32 v21, a57
	v_accvgpr_read_b32 v22, a73
	v_max3_f32 v10, |v10|, |v21|, |v22|
	v_accvgpr_read_b32 v23, a121
	v_accvgpr_read_b32 v24, a137
	v_max3_f32 v10, |v10|, |v23|, |v24|
	v_mov_b64_e32 v[44:45], v[48:49]
	v_accvgpr_read_b32 v25, a89
	v_max3_f32 v11, |v10|, |v25|, |v25|
	v_accvgpr_read_b32 v27, a26
	v_accvgpr_read_b32 v28, a42
	v_max3_f32 v10, |v44|, |v27|, |v28|
	v_accvgpr_read_b32 v29, a58
	v_accvgpr_read_b32 v30, a74
	v_max3_f32 v10, |v10|, |v29|, |v30|
	v_accvgpr_read_b32 v31, a122
	v_accvgpr_read_b32 v32, a138
	v_max3_f32 v10, |v10|, |v31|, |v32|
	v_accvgpr_read_b32 v33, a90
	v_max3_f32 v12, |v10|, |v33|, |v33|
	v_accvgpr_read_b32 v35, a27
	v_accvgpr_read_b32 v36, a43
	v_max3_f32 v10, |v45|, |v35|, |v36|
	v_accvgpr_read_b32 v37, a59
	v_accvgpr_read_b32 v38, a75
	v_max3_f32 v10, |v10|, |v37|, |v38|
	v_accvgpr_read_b32 v39, a123
	v_accvgpr_read_b32 v40, a139
	v_max3_f32 v10, |v10|, |v39|, |v40|
	v_accvgpr_read_b32 v41, a91
	v_max3_f32 v13, |v10|, |v41|, |v41|
	v_mov_b32_e32 v3, v42
	s_nop 1
	v_max_f32_dpp v8, v8, v8 quad_perm:[1,0,3,2] row_mask:0xf bank_mask:0xf
	v_max_f32_dpp v11, v11, v11 quad_perm:[1,0,3,2] row_mask:0xf bank_mask:0xf
	v_max_f32_dpp v12, v12, v12 quad_perm:[1,0,3,2] row_mask:0xf bank_mask:0xf
	v_max_f32_dpp v13, v13, v13 quad_perm:[1,0,3,2] row_mask:0xf bank_mask:0xf
	v_max_f32_dpp v8, v8, v8 quad_perm:[2,3,0,1] row_mask:0xf bank_mask:0xf
	v_max_f32_dpp v11, v11, v11 quad_perm:[2,3,0,1] row_mask:0xf bank_mask:0xf
	v_max_f32_dpp v12, v12, v12 quad_perm:[2,3,0,1] row_mask:0xf bank_mask:0xf
	v_max_f32_dpp v13, v13, v13 quad_perm:[2,3,0,1] row_mask:0xf bank_mask:0xf
	v_max_f32_dpp v8, v8, v8 row_half_mirror row_mask:0xf bank_mask:0xf
	v_max_f32_dpp v11, v11, v11 row_half_mirror row_mask:0xf bank_mask:0xf
	v_max_f32_dpp v12, v12, v12 row_half_mirror row_mask:0xf bank_mask:0xf
	v_max_f32_dpp v13, v13, v13 row_half_mirror row_mask:0xf bank_mask:0xf
	v_max_f32_dpp v8, v8, v8 row_mirror row_mask:0xf bank_mask:0xf
	v_max_f32_dpp v11, v11, v11 row_mirror row_mask:0xf bank_mask:0xf
	v_max_f32_dpp v12, v12, v12 row_mirror row_mask:0xf bank_mask:0xf
	v_max_f32_dpp v13, v13, v13 row_mirror row_mask:0xf bank_mask:0xf
	s_nop 0
	ds_swizzle_b32 v232, v8 offset:swizzle(SWAP,16)
	ds_swizzle_b32 v233, v11 offset:swizzle(SWAP,16)
	ds_swizzle_b32 v234, v12 offset:swizzle(SWAP,16)
	ds_swizzle_b32 v235, v13 offset:swizzle(SWAP,16)
	s_waitcnt lgkmcnt(0)
	v_max_f32_e32 v10, v8, v232
	v_rcp_f32_e32 v8, v10
	v_cmp_lt_f32_e32 vcc, 0, v10
	s_waitcnt lgkmcnt(0)
	v_max_f32_e32 v11, v11, v233
	v_mov_b32_e32 v18, v43
	s_mov_b64 s[6:7], 0x2000
	v_cndmask_b32_e32 v42, 0, v8, vcc
	v_mul_f32_e32 v3, v42, v3
	v_mul_f32_e32 v6, v42, v6
	v_cvt_pknorm_i16_f32 v6, v3, v6
	v_mul_f32_e32 v3, v42, v7
	v_mul_f32_e32 v7, v42, v9
	v_cvt_pknorm_i16_f32 v7, v3, v7
	v_pk_mul_f32 v[228:229], v[14:15], v[42:43] op_sel_hi:[1,0]
	v_pk_mul_f32 v[230:231], v[16:17], v[42:43] op_sel_hi:[1,0]
	v_cvt_pknorm_i16_f32 v8, v228, v229
	v_cvt_pknorm_i16_f32 v9, v230, v231
	v_rcp_f32_e32 v3, v11
	v_cmp_lt_f32_e32 vcc, 0, v11
	v_lshl_add_u64 v[14:15], v[4:5], 0, s[6:7]
	global_store_dwordx4 v[14:15], v[6:9], off sc0 sc1
	v_cndmask_b32_e32 v3, 0, v3, vcc
	v_pk_mul_f32 v[224:225], v[18:19], v[2:3] op_sel:[0,1] op_sel_hi:[1,1]
	v_pk_mul_f32 v[226:227], v[20:21], v[2:3] op_sel:[0,1] op_sel_hi:[1,1]
	v_cvt_pknorm_i16_f32 v6, v224, v225
	v_cvt_pknorm_i16_f32 v7, v226, v227
	v_pk_mul_f32 v[228:229], v[22:23], v[2:3] op_sel:[0,1] op_sel_hi:[1,1]
	v_pk_mul_f32 v[230:231], v[24:25], v[2:3] op_sel:[0,1] op_sel_hi:[1,1]
	v_cvt_pknorm_i16_f32 v8, v228, v229
	s_waitcnt lgkmcnt(0)
	v_max_f32_e32 v12, v12, v234
	v_cvt_pknorm_i16_f32 v9, v230, v231
	v_rcp_f32_e32 v3, v12
	s_mov_b64 s[6:7], 0x2200
	v_cmp_lt_f32_e32 vcc, 0, v12
	v_mov_b32_e32 v26, v44
	v_lshl_add_u64 v[14:15], v[4:5], 0, s[6:7]
	global_store_dwordx4 v[14:15], v[6:9], off sc0 sc1
	s_nop 1
	v_pk_mul_f32 v[6:7], v[10:11], s[4:5] op_sel_hi:[1,0]
	v_cndmask_b32_e32 v3, 0, v3, vcc
	global_store_dwordx2 v0, v[6:7], s[2:3] offset:64
	v_pk_mul_f32 v[224:225], v[26:27], v[2:3] op_sel:[0,1] op_sel_hi:[1,1]
	v_pk_mul_f32 v[226:227], v[28:29], v[2:3] op_sel:[0,1] op_sel_hi:[1,1]
	v_cvt_pknorm_i16_f32 v6, v224, v225
	v_cvt_pknorm_i16_f32 v7, v226, v227
	v_pk_mul_f32 v[228:229], v[30:31], v[2:3] op_sel:[0,1] op_sel_hi:[1,1]
	v_pk_mul_f32 v[230:231], v[32:33], v[2:3] op_sel:[0,1] op_sel_hi:[1,1]
	v_cvt_pknorm_i16_f32 v8, v228, v229
	s_waitcnt lgkmcnt(0)
	v_max_f32_e32 v13, v13, v235
	v_cvt_pknorm_i16_f32 v9, v230, v231
	v_rcp_f32_e32 v3, v13
	v_cmp_lt_f32_e32 vcc, 0, v13
	v_mov_b32_e32 v34, v45
	s_mov_b64 s[6:7], 0x2400
	v_cndmask_b32_e32 v3, 0, v3, vcc
	v_lshl_add_u64 v[10:11], v[4:5], 0, s[6:7]
	global_store_dwordx4 v[10:11], v[6:9], off sc0 sc1
	v_pk_mul_f32 v[224:225], v[34:35], v[2:3] op_sel:[0,1] op_sel_hi:[1,1]
	v_pk_mul_f32 v[226:227], v[36:37], v[2:3] op_sel:[0,1] op_sel_hi:[1,1]
	v_cvt_pknorm_i16_f32 v6, v224, v225
	v_cvt_pknorm_i16_f32 v7, v226, v227
	v_pk_mul_f32 v[228:229], v[38:39], v[2:3] op_sel:[0,1] op_sel_hi:[1,1]
	v_pk_mul_f32 v[230:231], v[40:41], v[2:3] op_sel:[0,1] op_sel_hi:[1,1]
	v_cvt_pknorm_i16_f32 v8, v228, v229
	s_mov_b64 s[6:7], 0x2600
	v_cvt_pknorm_i16_f32 v9, v230, v231
	v_lshl_add_u64 v[10:11], v[4:5], 0, s[6:7]
	global_store_dwordx4 v[10:11], v[6:9], off sc0 sc1
	s_nop 1
	v_pk_mul_f32 v[6:7], v[12:13], s[4:5] op_sel_hi:[1,0]
	v_mov_b64_e32 v[46:47], v[50:51]
	v_mov_b64_e32 v[48:49], v[52:53]
	global_store_dwordx2 v0, v[6:7], s[2:3] offset:72
	v_mov_b64_e32 v[32:33], v[46:47]
	v_accvgpr_read_b32 v6, a28
	v_accvgpr_read_b32 v7, a44
	v_max3_f32 v8, |v32|, |v6|, |v7|
	v_accvgpr_read_b32 v9, a60
	v_accvgpr_read_b32 v14, a76
	v_max3_f32 v8, |v8|, |v9|, |v14|
	v_accvgpr_read_b32 v15, a124
	v_accvgpr_read_b32 v16, a140
	v_max3_f32 v8, |v8|, |v15|, |v16|
	v_accvgpr_read_b32 v10, a92
	v_accvgpr_read_b32 v17, a92
	v_max3_f32 v8, |v8|, |v17|, |v10|
	v_accvgpr_read_b32 v19, a29
	v_accvgpr_read_b32 v20, a45
	v_max3_f32 v10, |v33|, |v19|, |v20|
	v_accvgpr_read_b32 v21, a61
	v_accvgpr_read_b32 v22, a77
	v_max3_f32 v10, |v10|, |v21|, |v22|
	v_accvgpr_read_b32 v23, a125
	v_accvgpr_read_b32 v24, a141
	v_max3_f32 v10, |v10|, |v23|, |v24|
	v_mov_b64_e32 v[34:35], v[48:49]
	v_accvgpr_read_b32 v25, a93
	v_max3_f32 v11, |v10|, |v25|, |v25|
	v_accvgpr_read_b32 v27, a30
	v_accvgpr_read_b32 v28, a46
	v_max3_f32 v10, |v34|, |v27|, |v28|
	v_accvgpr_read_b32 v29, a62
	v_accvgpr_read_b32 v30, a78
	v_max3_f32 v10, |v10|, |v29|, |v30|
	v_mov_b32_e32 v3, v32
	v_accvgpr_read_b32 v31, a126
	v_accvgpr_read_b32 v32, a142
	v_max3_f32 v10, |v10|, |v31|, |v32|
	v_mov_b32_e32 v18, v33
	v_mov_b32_e32 v26, v34
	v_accvgpr_read_b32 v33, a94
	v_max3_f32 v12, |v10|, |v33|, |v33|
	v_mov_b32_e32 v34, v35
	v_accvgpr_read_b32 v35, a31
	v_accvgpr_read_b32 v36, a47
	v_max3_f32 v10, |v34|, |v35|, |v36|
	v_accvgpr_read_b32 v37, a63
	v_accvgpr_read_b32 v38, a79
	v_max3_f32 v10, |v10|, |v37|, |v38|
	v_accvgpr_read_b32 v39, a127
	v_accvgpr_read_b32 v40, a143
	v_max3_f32 v10, |v10|, |v39|, |v40|
	v_accvgpr_read_b32 v41, a95
	v_max3_f32 v13, |v10|, |v41|, |v41|
	s_mov_b64 s[6:7], 0x3000
	s_nop 1
	v_max_f32_dpp v8, v8, v8 quad_perm:[1,0,3,2] row_mask:0xf bank_mask:0xf
	v_max_f32_dpp v11, v11, v11 quad_perm:[1,0,3,2] row_mask:0xf bank_mask:0xf
	v_max_f32_dpp v12, v12, v12 quad_perm:[1,0,3,2] row_mask:0xf bank_mask:0xf
	v_max_f32_dpp v13, v13, v13 quad_perm:[1,0,3,2] row_mask:0xf bank_mask:0xf
	v_max_f32_dpp v8, v8, v8 quad_perm:[2,3,0,1] row_mask:0xf bank_mask:0xf
	v_max_f32_dpp v11, v11, v11 quad_perm:[2,3,0,1] row_mask:0xf bank_mask:0xf
	v_max_f32_dpp v12, v12, v12 quad_perm:[2,3,0,1] row_mask:0xf bank_mask:0xf
	v_max_f32_dpp v13, v13, v13 quad_perm:[2,3,0,1] row_mask:0xf bank_mask:0xf
	v_max_f32_dpp v8, v8, v8 row_half_mirror row_mask:0xf bank_mask:0xf
	v_max_f32_dpp v11, v11, v11 row_half_mirror row_mask:0xf bank_mask:0xf
	v_max_f32_dpp v12, v12, v12 row_half_mirror row_mask:0xf bank_mask:0xf
	v_max_f32_dpp v13, v13, v13 row_half_mirror row_mask:0xf bank_mask:0xf
	v_max_f32_dpp v8, v8, v8 row_mirror row_mask:0xf bank_mask:0xf
	v_max_f32_dpp v11, v11, v11 row_mirror row_mask:0xf bank_mask:0xf
	v_max_f32_dpp v12, v12, v12 row_mirror row_mask:0xf bank_mask:0xf
	v_max_f32_dpp v13, v13, v13 row_mirror row_mask:0xf bank_mask:0xf
	s_nop 0
	ds_swizzle_b32 v232, v8 offset:swizzle(SWAP,16)
	ds_swizzle_b32 v233, v11 offset:swizzle(SWAP,16)
	ds_swizzle_b32 v234, v12 offset:swizzle(SWAP,16)
	ds_swizzle_b32 v235, v13 offset:swizzle(SWAP,16)
	s_waitcnt lgkmcnt(0)
	v_max_f32_e32 v10, v8, v232
	v_rcp_f32_e32 v8, v10
	v_cmp_lt_f32_e32 vcc, 0, v10
	s_waitcnt lgkmcnt(0)
	v_max_f32_e32 v11, v11, v233
	s_waitcnt lgkmcnt(0)
	v_max_f32_e32 v12, v12, v234
	v_cndmask_b32_e32 v42, 0, v8, vcc
	v_mul_f32_e32 v3, v42, v3
	v_mul_f32_e32 v6, v42, v6
	v_cvt_pknorm_i16_f32 v6, v3, v6
	v_mul_f32_e32 v3, v42, v7
	v_mul_f32_e32 v7, v42, v9
	v_cvt_pknorm_i16_f32 v7, v3, v7
	v_pk_mul_f32 v[224:225], v[14:15], v[42:43] op_sel_hi:[1,0]
	v_pk_mul_f32 v[226:227], v[16:17], v[42:43] op_sel_hi:[1,0]
	v_cvt_pknorm_i16_f32 v8, v224, v225
	v_cvt_pknorm_i16_f32 v9, v226, v227
	v_rcp_f32_e32 v3, v11
	v_cmp_lt_f32_e32 vcc, 0, v11
	v_lshl_add_u64 v[14:15], v[4:5], 0, s[6:7]
	global_store_dwordx4 v[14:15], v[6:9], off sc0 sc1
	s_mov_b64 s[6:7], 0x3200
	v_cndmask_b32_e32 v3, 0, v3, vcc
	v_pk_mul_f32 v[228:229], v[18:19], v[2:3] op_sel:[0,1] op_sel_hi:[1,1]
	v_pk_mul_f32 v[230:231], v[20:21], v[2:3] op_sel:[0,1] op_sel_hi:[1,1]
	v_cvt_pknorm_i16_f32 v6, v228, v229
	v_cvt_pknorm_i16_f32 v7, v230, v231
	v_pk_mul_f32 v[224:225], v[22:23], v[2:3] op_sel:[0,1] op_sel_hi:[1,1]
	v_pk_mul_f32 v[226:227], v[24:25], v[2:3] op_sel:[0,1] op_sel_hi:[1,1]
	v_cvt_pknorm_i16_f32 v8, v224, v225
	v_cvt_pknorm_i16_f32 v9, v226, v227
	v_rcp_f32_e32 v3, v12
	v_cmp_lt_f32_e32 vcc, 0, v12
	v_lshl_add_u64 v[14:15], v[4:5], 0, s[6:7]
	global_store_dwordx4 v[14:15], v[6:9], off sc0 sc1
	s_nop 1
	v_pk_mul_f32 v[6:7], v[10:11], s[4:5] op_sel_hi:[1,0]
	v_cndmask_b32_e32 v3, 0, v3, vcc
	global_store_dwordx2 v0, v[6:7], s[2:3] offset:96
	v_pk_mul_f32 v[228:229], v[26:27], v[2:3] op_sel:[0,1] op_sel_hi:[1,1]
	v_pk_mul_f32 v[230:231], v[28:29], v[2:3] op_sel:[0,1] op_sel_hi:[1,1]
	v_cvt_pknorm_i16_f32 v6, v228, v229
	v_cvt_pknorm_i16_f32 v7, v230, v231
	v_pk_mul_f32 v[224:225], v[30:31], v[2:3] op_sel:[0,1] op_sel_hi:[1,1]
	v_pk_mul_f32 v[226:227], v[32:33], v[2:3] op_sel:[0,1] op_sel_hi:[1,1]
	v_cvt_pknorm_i16_f32 v8, v224, v225
	s_waitcnt lgkmcnt(0)
	v_max_f32_e32 v13, v13, v235
	v_cvt_pknorm_i16_f32 v9, v226, v227
	v_rcp_f32_e32 v3, v13
	v_cmp_lt_f32_e32 vcc, 0, v13
	s_mov_b64 s[6:7], 0x3400
	v_lshl_add_u64 v[10:11], v[4:5], 0, s[6:7]
	v_cndmask_b32_e32 v3, 0, v3, vcc
	global_store_dwordx4 v[10:11], v[6:9], off sc0 sc1
	v_pk_mul_f32 v[228:229], v[34:35], v[2:3] op_sel:[0,1] op_sel_hi:[1,1]
	v_pk_mul_f32 v[230:231], v[36:37], v[2:3] op_sel:[0,1] op_sel_hi:[1,1]
	v_cvt_pknorm_i16_f32 v6, v228, v229
	v_cvt_pknorm_i16_f32 v7, v230, v231
	v_pk_mul_f32 v[224:225], v[38:39], v[2:3] op_sel:[0,1] op_sel_hi:[1,1]
	v_pk_mul_f32 v[226:227], v[40:41], v[2:3] op_sel:[0,1] op_sel_hi:[1,1]
	v_cvt_pknorm_i16_f32 v8, v224, v225
	s_mov_b64 s[6:7], 0x3600
	v_cvt_pknorm_i16_f32 v9, v226, v227
	v_lshl_add_u64 v[10:11], v[4:5], 0, s[6:7]
	global_store_dwordx4 v[10:11], v[6:9], off sc0 sc1
	s_nop 1
	v_pk_mul_f32 v[6:7], v[12:13], s[4:5] op_sel_hi:[1,0]
	global_store_dwordx2 v0, v[6:7], s[2:3] offset:104
	v_accvgpr_read_b32 v3, a240
	v_accvgpr_read_b32 v6, a224
	v_accvgpr_read_b32 v7, a208
	v_max3_f32 v8, |v3|, |v6|, |v7|
	v_accvgpr_read_b32 v9, a192
	v_accvgpr_read_b32 v14, a176
	v_max3_f32 v8, |v8|, |v9|, |v14|
	v_accvgpr_read_b32 v15, a160
	v_accvgpr_read_b32 v16, a144
	v_max3_f32 v8, |v8|, |v15|, |v16|
	v_accvgpr_read_b32 v10, a96
	v_accvgpr_read_b32 v17, a96
	v_max3_f32 v8, |v8|, |v17|, |v10|
	v_accvgpr_read_b32 v18, a241
	v_accvgpr_read_b32 v19, a225
	v_accvgpr_read_b32 v20, a209
	v_max3_f32 v10, |v18|, |v19|, |v20|
	v_accvgpr_read_b32 v21, a193
	v_accvgpr_read_b32 v22, a177
	v_max3_f32 v10, |v10|, |v21|, |v22|
	v_accvgpr_read_b32 v23, a161
	v_accvgpr_read_b32 v24, a145
	v_max3_f32 v10, |v10|, |v23|, |v24|
	v_accvgpr_read_b32 v25, a97
	v_max3_f32 v11, |v10|, |v25|, |v25|
	v_accvgpr_read_b32 v26, a242
	v_accvgpr_read_b32 v27, a226
	v_accvgpr_read_b32 v28, a210
	v_max3_f32 v10, |v26|, |v27|, |v28|
	v_accvgpr_read_b32 v29, a194
	v_accvgpr_read_b32 v30, a178
	v_max3_f32 v10, |v10|, |v29|, |v30|
	v_accvgpr_read_b32 v31, a162
	v_accvgpr_read_b32 v32, a146
	v_max3_f32 v10, |v10|, |v31|, |v32|
	v_accvgpr_read_b32 v33, a98
	v_max3_f32 v12, |v10|, |v33|, |v33|
	v_accvgpr_read_b32 v34, a243
	v_accvgpr_read_b32 v35, a227
	v_accvgpr_read_b32 v36, a211
	v_max3_f32 v10, |v34|, |v35|, |v36|
	v_accvgpr_read_b32 v37, a195
	v_accvgpr_read_b32 v38, a179
	v_max3_f32 v10, |v10|, |v37|, |v38|
	v_accvgpr_read_b32 v39, a163
	v_accvgpr_read_b32 v40, a147
	v_max3_f32 v10, |v10|, |v39|, |v40|
	v_accvgpr_read_b32 v41, a99
	v_max3_f32 v13, |v10|, |v41|, |v41|
	s_mov_b64 s[6:7], 0x4000
	s_nop 1
	v_max_f32_dpp v8, v8, v8 quad_perm:[1,0,3,2] row_mask:0xf bank_mask:0xf
	v_max_f32_dpp v11, v11, v11 quad_perm:[1,0,3,2] row_mask:0xf bank_mask:0xf
	v_max_f32_dpp v12, v12, v12 quad_perm:[1,0,3,2] row_mask:0xf bank_mask:0xf
	v_max_f32_dpp v13, v13, v13 quad_perm:[1,0,3,2] row_mask:0xf bank_mask:0xf
	v_max_f32_dpp v8, v8, v8 quad_perm:[2,3,0,1] row_mask:0xf bank_mask:0xf
	v_max_f32_dpp v11, v11, v11 quad_perm:[2,3,0,1] row_mask:0xf bank_mask:0xf
	v_max_f32_dpp v12, v12, v12 quad_perm:[2,3,0,1] row_mask:0xf bank_mask:0xf
	v_max_f32_dpp v13, v13, v13 quad_perm:[2,3,0,1] row_mask:0xf bank_mask:0xf
	v_max_f32_dpp v8, v8, v8 row_half_mirror row_mask:0xf bank_mask:0xf
	v_max_f32_dpp v11, v11, v11 row_half_mirror row_mask:0xf bank_mask:0xf
	v_max_f32_dpp v12, v12, v12 row_half_mirror row_mask:0xf bank_mask:0xf
	v_max_f32_dpp v13, v13, v13 row_half_mirror row_mask:0xf bank_mask:0xf
	v_max_f32_dpp v8, v8, v8 row_mirror row_mask:0xf bank_mask:0xf
	v_max_f32_dpp v11, v11, v11 row_mirror row_mask:0xf bank_mask:0xf
	v_max_f32_dpp v12, v12, v12 row_mirror row_mask:0xf bank_mask:0xf
	v_max_f32_dpp v13, v13, v13 row_mirror row_mask:0xf bank_mask:0xf
	s_nop 0
	ds_swizzle_b32 v232, v8 offset:swizzle(SWAP,16)
	ds_swizzle_b32 v233, v11 offset:swizzle(SWAP,16)
	ds_swizzle_b32 v234, v12 offset:swizzle(SWAP,16)
	ds_swizzle_b32 v235, v13 offset:swizzle(SWAP,16)
	s_waitcnt lgkmcnt(0)
	v_max_f32_e32 v10, v8, v232
	v_rcp_f32_e32 v8, v10
	v_cmp_lt_f32_e32 vcc, 0, v10
	s_waitcnt lgkmcnt(0)
	v_max_f32_e32 v11, v11, v233
	s_waitcnt lgkmcnt(0)
	v_max_f32_e32 v12, v12, v234
	v_cndmask_b32_e32 v42, 0, v8, vcc
	v_mul_f32_e32 v3, v42, v3
	v_mul_f32_e32 v6, v42, v6
	v_cvt_pknorm_i16_f32 v6, v3, v6
	v_mul_f32_e32 v3, v42, v7
	v_mul_f32_e32 v7, v42, v9
	v_cvt_pknorm_i16_f32 v7, v3, v7
	v_pk_mul_f32 v[228:229], v[14:15], v[42:43] op_sel_hi:[1,0]
	v_pk_mul_f32 v[230:231], v[16:17], v[42:43] op_sel_hi:[1,0]
	v_cvt_pknorm_i16_f32 v8, v228, v229
	v_cvt_pknorm_i16_f32 v9, v230, v231
	v_rcp_f32_e32 v3, v11
	v_cmp_lt_f32_e32 vcc, 0, v11
	v_lshl_add_u64 v[14:15], v[4:5], 0, s[6:7]
	global_store_dwordx4 v[14:15], v[6:9], off sc0 sc1
	s_mov_b64 s[6:7], 0x4200
	v_cndmask_b32_e32 v3, 0, v3, vcc
	v_pk_mul_f32 v[224:225], v[18:19], v[2:3] op_sel:[0,1] op_sel_hi:[1,1]
	v_pk_mul_f32 v[226:227], v[20:21], v[2:3] op_sel:[0,1] op_sel_hi:[1,1]
	v_cvt_pknorm_i16_f32 v6, v224, v225
	v_cvt_pknorm_i16_f32 v7, v226, v227
	v_pk_mul_f32 v[228:229], v[22:23], v[2:3] op_sel:[0,1] op_sel_hi:[1,1]
	v_pk_mul_f32 v[230:231], v[24:25], v[2:3] op_sel:[0,1] op_sel_hi:[1,1]
	v_cvt_pknorm_i16_f32 v8, v228, v229
	v_cvt_pknorm_i16_f32 v9, v230, v231
	v_rcp_f32_e32 v3, v12
	v_cmp_lt_f32_e32 vcc, 0, v12
	v_lshl_add_u64 v[14:15], v[4:5], 0, s[6:7]
	global_store_dwordx4 v[14:15], v[6:9], off sc0 sc1
	s_nop 1
	v_pk_mul_f32 v[6:7], v[10:11], s[4:5] op_sel_hi:[1,0]
	v_cndmask_b32_e32 v3, 0, v3, vcc
	global_store_dwordx2 v0, v[6:7], s[2:3] offset:128
	v_pk_mul_f32 v[224:225], v[26:27], v[2:3] op_sel:[0,1] op_sel_hi:[1,1]
	v_pk_mul_f32 v[226:227], v[28:29], v[2:3] op_sel:[0,1] op_sel_hi:[1,1]
	v_cvt_pknorm_i16_f32 v6, v224, v225
	v_cvt_pknorm_i16_f32 v7, v226, v227
	v_pk_mul_f32 v[228:229], v[30:31], v[2:3] op_sel:[0,1] op_sel_hi:[1,1]
	v_pk_mul_f32 v[230:231], v[32:33], v[2:3] op_sel:[0,1] op_sel_hi:[1,1]
	v_cvt_pknorm_i16_f32 v8, v228, v229
	s_waitcnt lgkmcnt(0)
	v_max_f32_e32 v13, v13, v235
	v_cvt_pknorm_i16_f32 v9, v230, v231
	v_rcp_f32_e32 v3, v13
	v_cmp_lt_f32_e32 vcc, 0, v13
	s_mov_b64 s[6:7], 0x4400
	v_lshl_add_u64 v[10:11], v[4:5], 0, s[6:7]
	v_cndmask_b32_e32 v3, 0, v3, vcc
	global_store_dwordx4 v[10:11], v[6:9], off sc0 sc1
	v_pk_mul_f32 v[224:225], v[34:35], v[2:3] op_sel:[0,1] op_sel_hi:[1,1]
	v_pk_mul_f32 v[226:227], v[36:37], v[2:3] op_sel:[0,1] op_sel_hi:[1,1]
	v_cvt_pknorm_i16_f32 v6, v224, v225
	v_cvt_pknorm_i16_f32 v7, v226, v227
	v_pk_mul_f32 v[228:229], v[38:39], v[2:3] op_sel:[0,1] op_sel_hi:[1,1]
	v_pk_mul_f32 v[230:231], v[40:41], v[2:3] op_sel:[0,1] op_sel_hi:[1,1]
	v_cvt_pknorm_i16_f32 v8, v228, v229
	s_mov_b64 s[6:7], 0x4600
	v_cvt_pknorm_i16_f32 v9, v230, v231
	v_lshl_add_u64 v[10:11], v[4:5], 0, s[6:7]
	global_store_dwordx4 v[10:11], v[6:9], off sc0 sc1
	s_nop 1
	v_pk_mul_f32 v[6:7], v[12:13], s[4:5] op_sel_hi:[1,0]
	global_store_dwordx2 v0, v[6:7], s[2:3] offset:136
	v_accvgpr_read_b32 v3, a244
	v_accvgpr_read_b32 v6, a228
	v_accvgpr_read_b32 v7, a212
	v_max3_f32 v8, |v3|, |v6|, |v7|
	v_accvgpr_read_b32 v9, a196
	v_accvgpr_read_b32 v14, a180
	v_max3_f32 v8, |v8|, |v9|, |v14|
	v_accvgpr_read_b32 v15, a164
	v_accvgpr_read_b32 v16, a148
	v_max3_f32 v8, |v8|, |v15|, |v16|
	v_accvgpr_read_b32 v10, a100
	v_accvgpr_read_b32 v17, a100
	v_max3_f32 v8, |v8|, |v17|, |v10|
	v_accvgpr_read_b32 v18, a245
	v_accvgpr_read_b32 v19, a229
	v_accvgpr_read_b32 v20, a213
	v_max3_f32 v10, |v18|, |v19|, |v20|
	v_accvgpr_read_b32 v21, a197
	v_accvgpr_read_b32 v22, a181
	v_max3_f32 v10, |v10|, |v21|, |v22|
	v_accvgpr_read_b32 v23, a165
	v_accvgpr_read_b32 v24, a149
	v_max3_f32 v10, |v10|, |v23|, |v24|
	v_accvgpr_read_b32 v25, a101
	v_max3_f32 v11, |v10|, |v25|, |v25|
	v_accvgpr_read_b32 v26, a246
	v_accvgpr_read_b32 v27, a230
	v_accvgpr_read_b32 v28, a214
	v_max3_f32 v10, |v26|, |v27|, |v28|
	v_accvgpr_read_b32 v29, a198
	v_accvgpr_read_b32 v30, a182
	v_max3_f32 v10, |v10|, |v29|, |v30|
	v_accvgpr_read_b32 v31, a166
	v_accvgpr_read_b32 v32, a150
	v_max3_f32 v10, |v10|, |v31|, |v32|
	v_accvgpr_read_b32 v33, a102
	v_max3_f32 v12, |v10|, |v33|, |v33|
	v_accvgpr_read_b32 v34, a247
	v_accvgpr_read_b32 v35, a231
	v_accvgpr_read_b32 v36, a215
	v_max3_f32 v10, |v34|, |v35|, |v36|
	v_accvgpr_read_b32 v37, a199
	v_accvgpr_read_b32 v38, a183
	v_max3_f32 v10, |v10|, |v37|, |v38|
	v_accvgpr_read_b32 v39, a167
	v_accvgpr_read_b32 v40, a151
	v_max3_f32 v10, |v10|, |v39|, |v40|
	v_accvgpr_read_b32 v41, a103
	v_max3_f32 v13, |v10|, |v41|, |v41|
	s_mov_b64 s[6:7], 0x5000
	s_nop 1
	v_max_f32_dpp v8, v8, v8 quad_perm:[1,0,3,2] row_mask:0xf bank_mask:0xf
	v_max_f32_dpp v11, v11, v11 quad_perm:[1,0,3,2] row_mask:0xf bank_mask:0xf
	v_max_f32_dpp v12, v12, v12 quad_perm:[1,0,3,2] row_mask:0xf bank_mask:0xf
	v_max_f32_dpp v13, v13, v13 quad_perm:[1,0,3,2] row_mask:0xf bank_mask:0xf
	v_max_f32_dpp v8, v8, v8 quad_perm:[2,3,0,1] row_mask:0xf bank_mask:0xf
	v_max_f32_dpp v11, v11, v11 quad_perm:[2,3,0,1] row_mask:0xf bank_mask:0xf
	v_max_f32_dpp v12, v12, v12 quad_perm:[2,3,0,1] row_mask:0xf bank_mask:0xf
	v_max_f32_dpp v13, v13, v13 quad_perm:[2,3,0,1] row_mask:0xf bank_mask:0xf
	v_max_f32_dpp v8, v8, v8 row_half_mirror row_mask:0xf bank_mask:0xf
	v_max_f32_dpp v11, v11, v11 row_half_mirror row_mask:0xf bank_mask:0xf
	v_max_f32_dpp v12, v12, v12 row_half_mirror row_mask:0xf bank_mask:0xf
	v_max_f32_dpp v13, v13, v13 row_half_mirror row_mask:0xf bank_mask:0xf
	v_max_f32_dpp v8, v8, v8 row_mirror row_mask:0xf bank_mask:0xf
	v_max_f32_dpp v11, v11, v11 row_mirror row_mask:0xf bank_mask:0xf
	v_max_f32_dpp v12, v12, v12 row_mirror row_mask:0xf bank_mask:0xf
	v_max_f32_dpp v13, v13, v13 row_mirror row_mask:0xf bank_mask:0xf
	s_nop 0
	ds_swizzle_b32 v232, v8 offset:swizzle(SWAP,16)
	ds_swizzle_b32 v233, v11 offset:swizzle(SWAP,16)
	ds_swizzle_b32 v234, v12 offset:swizzle(SWAP,16)
	ds_swizzle_b32 v235, v13 offset:swizzle(SWAP,16)
	s_waitcnt lgkmcnt(0)
	v_max_f32_e32 v10, v8, v232
	v_rcp_f32_e32 v8, v10
	v_cmp_lt_f32_e32 vcc, 0, v10
	s_waitcnt lgkmcnt(0)
	v_max_f32_e32 v11, v11, v233
	s_waitcnt lgkmcnt(0)
	v_max_f32_e32 v12, v12, v234
	v_cndmask_b32_e32 v42, 0, v8, vcc
	v_mul_f32_e32 v3, v42, v3
	v_mul_f32_e32 v6, v42, v6
	v_cvt_pknorm_i16_f32 v6, v3, v6
	v_mul_f32_e32 v3, v42, v7
	v_mul_f32_e32 v7, v42, v9
	v_cvt_pknorm_i16_f32 v7, v3, v7
	v_pk_mul_f32 v[224:225], v[14:15], v[42:43] op_sel_hi:[1,0]
	v_pk_mul_f32 v[226:227], v[16:17], v[42:43] op_sel_hi:[1,0]
	v_cvt_pknorm_i16_f32 v8, v224, v225
	v_cvt_pknorm_i16_f32 v9, v226, v227
	v_rcp_f32_e32 v3, v11
	v_cmp_lt_f32_e32 vcc, 0, v11
	v_lshl_add_u64 v[14:15], v[4:5], 0, s[6:7]
	global_store_dwordx4 v[14:15], v[6:9], off sc0 sc1
	s_mov_b64 s[6:7], 0x5200
	v_cndmask_b32_e32 v3, 0, v3, vcc
	v_pk_mul_f32 v[228:229], v[18:19], v[2:3] op_sel:[0,1] op_sel_hi:[1,1]
	v_pk_mul_f32 v[230:231], v[20:21], v[2:3] op_sel:[0,1] op_sel_hi:[1,1]
	v_cvt_pknorm_i16_f32 v6, v228, v229
	v_cvt_pknorm_i16_f32 v7, v230, v231
	v_pk_mul_f32 v[224:225], v[22:23], v[2:3] op_sel:[0,1] op_sel_hi:[1,1]
	v_pk_mul_f32 v[226:227], v[24:25], v[2:3] op_sel:[0,1] op_sel_hi:[1,1]
	v_cvt_pknorm_i16_f32 v8, v224, v225
	v_cvt_pknorm_i16_f32 v9, v226, v227
	v_rcp_f32_e32 v3, v12
	v_cmp_lt_f32_e32 vcc, 0, v12
	v_lshl_add_u64 v[14:15], v[4:5], 0, s[6:7]
	global_store_dwordx4 v[14:15], v[6:9], off sc0 sc1
	s_nop 1
	v_pk_mul_f32 v[6:7], v[10:11], s[4:5] op_sel_hi:[1,0]
	v_cndmask_b32_e32 v3, 0, v3, vcc
	global_store_dwordx2 v0, v[6:7], s[2:3] offset:160
	v_pk_mul_f32 v[228:229], v[26:27], v[2:3] op_sel:[0,1] op_sel_hi:[1,1]
	v_pk_mul_f32 v[230:231], v[28:29], v[2:3] op_sel:[0,1] op_sel_hi:[1,1]
	v_cvt_pknorm_i16_f32 v6, v228, v229
	v_cvt_pknorm_i16_f32 v7, v230, v231
	v_pk_mul_f32 v[224:225], v[30:31], v[2:3] op_sel:[0,1] op_sel_hi:[1,1]
	v_pk_mul_f32 v[226:227], v[32:33], v[2:3] op_sel:[0,1] op_sel_hi:[1,1]
	v_cvt_pknorm_i16_f32 v8, v224, v225
	s_waitcnt lgkmcnt(0)
	v_max_f32_e32 v13, v13, v235
	v_cvt_pknorm_i16_f32 v9, v226, v227
	v_rcp_f32_e32 v3, v13
	v_cmp_lt_f32_e32 vcc, 0, v13
	s_mov_b64 s[6:7], 0x5400
	v_lshl_add_u64 v[10:11], v[4:5], 0, s[6:7]
	v_cndmask_b32_e32 v3, 0, v3, vcc
	global_store_dwordx4 v[10:11], v[6:9], off sc0 sc1
	v_pk_mul_f32 v[228:229], v[34:35], v[2:3] op_sel:[0,1] op_sel_hi:[1,1]
	v_pk_mul_f32 v[230:231], v[36:37], v[2:3] op_sel:[0,1] op_sel_hi:[1,1]
	v_cvt_pknorm_i16_f32 v6, v228, v229
	v_cvt_pknorm_i16_f32 v7, v230, v231
	v_pk_mul_f32 v[224:225], v[38:39], v[2:3] op_sel:[0,1] op_sel_hi:[1,1]
	v_pk_mul_f32 v[226:227], v[40:41], v[2:3] op_sel:[0,1] op_sel_hi:[1,1]
	v_cvt_pknorm_i16_f32 v8, v224, v225
	s_mov_b64 s[6:7], 0x5600
	v_cvt_pknorm_i16_f32 v9, v226, v227
	v_lshl_add_u64 v[10:11], v[4:5], 0, s[6:7]
	global_store_dwordx4 v[10:11], v[6:9], off sc0 sc1
	s_nop 1
	v_pk_mul_f32 v[6:7], v[12:13], s[4:5] op_sel_hi:[1,0]
	global_store_dwordx2 v0, v[6:7], s[2:3] offset:168
	v_accvgpr_read_b32 v3, a248
	v_accvgpr_read_b32 v6, a232
	v_accvgpr_read_b32 v7, a216
	v_max3_f32 v8, |v3|, |v6|, |v7|
	v_accvgpr_read_b32 v9, a200
	v_accvgpr_read_b32 v14, a184
	v_max3_f32 v8, |v8|, |v9|, |v14|
	v_accvgpr_read_b32 v15, a168
	v_accvgpr_read_b32 v16, a152
	v_max3_f32 v8, |v8|, |v15|, |v16|
	v_accvgpr_read_b32 v10, a104
	v_accvgpr_read_b32 v17, a104
	v_max3_f32 v8, |v8|, |v17|, |v10|
	v_accvgpr_read_b32 v18, a249
	v_accvgpr_read_b32 v19, a233
	v_accvgpr_read_b32 v20, a217
	v_max3_f32 v10, |v18|, |v19|, |v20|
	v_accvgpr_read_b32 v21, a201
	v_accvgpr_read_b32 v22, a185
	v_max3_f32 v10, |v10|, |v21|, |v22|
	v_accvgpr_read_b32 v23, a169
	v_accvgpr_read_b32 v24, a153
	v_max3_f32 v10, |v10|, |v23|, |v24|
	v_accvgpr_read_b32 v25, a105
	v_max3_f32 v11, |v10|, |v25|, |v25|
	v_accvgpr_read_b32 v26, a250
	v_accvgpr_read_b32 v27, a234
	v_accvgpr_read_b32 v28, a218
	v_max3_f32 v10, |v26|, |v27|, |v28|
	v_accvgpr_read_b32 v29, a202
	v_accvgpr_read_b32 v30, a186
	v_max3_f32 v10, |v10|, |v29|, |v30|
	v_accvgpr_read_b32 v31, a170
	v_accvgpr_read_b32 v32, a154
	v_max3_f32 v10, |v10|, |v31|, |v32|
	v_accvgpr_read_b32 v33, a106
	v_max3_f32 v12, |v10|, |v33|, |v33|
	v_accvgpr_read_b32 v34, a251
	v_accvgpr_read_b32 v35, a235
	v_accvgpr_read_b32 v36, a219
	v_max3_f32 v10, |v34|, |v35|, |v36|
	v_accvgpr_read_b32 v37, a203
	v_accvgpr_read_b32 v38, a187
	v_max3_f32 v10, |v10|, |v37|, |v38|
	v_accvgpr_read_b32 v39, a171
	v_accvgpr_read_b32 v40, a155
	v_max3_f32 v10, |v10|, |v39|, |v40|
	v_accvgpr_read_b32 v41, a107
	v_max3_f32 v13, |v10|, |v41|, |v41|
	s_mov_b64 s[6:7], 0x6000
	s_nop 1
	v_max_f32_dpp v8, v8, v8 quad_perm:[1,0,3,2] row_mask:0xf bank_mask:0xf
	v_max_f32_dpp v11, v11, v11 quad_perm:[1,0,3,2] row_mask:0xf bank_mask:0xf
	v_max_f32_dpp v12, v12, v12 quad_perm:[1,0,3,2] row_mask:0xf bank_mask:0xf
	v_max_f32_dpp v13, v13, v13 quad_perm:[1,0,3,2] row_mask:0xf bank_mask:0xf
	v_max_f32_dpp v8, v8, v8 quad_perm:[2,3,0,1] row_mask:0xf bank_mask:0xf
	v_max_f32_dpp v11, v11, v11 quad_perm:[2,3,0,1] row_mask:0xf bank_mask:0xf
	v_max_f32_dpp v12, v12, v12 quad_perm:[2,3,0,1] row_mask:0xf bank_mask:0xf
	v_max_f32_dpp v13, v13, v13 quad_perm:[2,3,0,1] row_mask:0xf bank_mask:0xf
	v_max_f32_dpp v8, v8, v8 row_half_mirror row_mask:0xf bank_mask:0xf
	v_max_f32_dpp v11, v11, v11 row_half_mirror row_mask:0xf bank_mask:0xf
	v_max_f32_dpp v12, v12, v12 row_half_mirror row_mask:0xf bank_mask:0xf
	v_max_f32_dpp v13, v13, v13 row_half_mirror row_mask:0xf bank_mask:0xf
	v_max_f32_dpp v8, v8, v8 row_mirror row_mask:0xf bank_mask:0xf
	v_max_f32_dpp v11, v11, v11 row_mirror row_mask:0xf bank_mask:0xf
	v_max_f32_dpp v12, v12, v12 row_mirror row_mask:0xf bank_mask:0xf
	v_max_f32_dpp v13, v13, v13 row_mirror row_mask:0xf bank_mask:0xf
	s_nop 0
	ds_swizzle_b32 v232, v8 offset:swizzle(SWAP,16)
	ds_swizzle_b32 v233, v11 offset:swizzle(SWAP,16)
	ds_swizzle_b32 v234, v12 offset:swizzle(SWAP,16)
	ds_swizzle_b32 v235, v13 offset:swizzle(SWAP,16)
	s_waitcnt lgkmcnt(0)
	v_max_f32_e32 v10, v8, v232
	v_rcp_f32_e32 v8, v10
	v_cmp_lt_f32_e32 vcc, 0, v10
	s_waitcnt lgkmcnt(0)
	v_max_f32_e32 v11, v11, v233
	s_waitcnt lgkmcnt(0)
	v_max_f32_e32 v12, v12, v234
	v_cndmask_b32_e32 v42, 0, v8, vcc
	v_mul_f32_e32 v3, v42, v3
	v_mul_f32_e32 v6, v42, v6
	v_cvt_pknorm_i16_f32 v6, v3, v6
	v_mul_f32_e32 v3, v42, v7
	v_mul_f32_e32 v7, v42, v9
	v_cvt_pknorm_i16_f32 v7, v3, v7
	v_pk_mul_f32 v[228:229], v[14:15], v[42:43] op_sel_hi:[1,0]
	v_pk_mul_f32 v[230:231], v[16:17], v[42:43] op_sel_hi:[1,0]
	v_cvt_pknorm_i16_f32 v8, v228, v229
	v_cvt_pknorm_i16_f32 v9, v230, v231
	v_rcp_f32_e32 v3, v11
	v_cmp_lt_f32_e32 vcc, 0, v11
	v_lshl_add_u64 v[14:15], v[4:5], 0, s[6:7]
	global_store_dwordx4 v[14:15], v[6:9], off sc0 sc1
	s_mov_b64 s[6:7], 0x6200
	v_cndmask_b32_e32 v3, 0, v3, vcc
	v_pk_mul_f32 v[224:225], v[18:19], v[2:3] op_sel:[0,1] op_sel_hi:[1,1]
	v_pk_mul_f32 v[226:227], v[20:21], v[2:3] op_sel:[0,1] op_sel_hi:[1,1]
	v_cvt_pknorm_i16_f32 v6, v224, v225
	v_cvt_pknorm_i16_f32 v7, v226, v227
	v_pk_mul_f32 v[228:229], v[22:23], v[2:3] op_sel:[0,1] op_sel_hi:[1,1]
	v_pk_mul_f32 v[230:231], v[24:25], v[2:3] op_sel:[0,1] op_sel_hi:[1,1]
	v_cvt_pknorm_i16_f32 v8, v228, v229
	v_cvt_pknorm_i16_f32 v9, v230, v231
	v_rcp_f32_e32 v3, v12
	v_cmp_lt_f32_e32 vcc, 0, v12
	v_lshl_add_u64 v[14:15], v[4:5], 0, s[6:7]
	global_store_dwordx4 v[14:15], v[6:9], off sc0 sc1
	s_nop 1
	v_pk_mul_f32 v[6:7], v[10:11], s[4:5] op_sel_hi:[1,0]
	v_cndmask_b32_e32 v3, 0, v3, vcc
	global_store_dwordx2 v0, v[6:7], s[2:3] offset:192
	v_pk_mul_f32 v[224:225], v[26:27], v[2:3] op_sel:[0,1] op_sel_hi:[1,1]
	v_pk_mul_f32 v[226:227], v[28:29], v[2:3] op_sel:[0,1] op_sel_hi:[1,1]
	v_cvt_pknorm_i16_f32 v6, v224, v225
	v_cvt_pknorm_i16_f32 v7, v226, v227
	v_pk_mul_f32 v[228:229], v[30:31], v[2:3] op_sel:[0,1] op_sel_hi:[1,1]
	v_pk_mul_f32 v[230:231], v[32:33], v[2:3] op_sel:[0,1] op_sel_hi:[1,1]
	v_cvt_pknorm_i16_f32 v8, v228, v229
	s_waitcnt lgkmcnt(0)
	v_max_f32_e32 v13, v13, v235
	v_cvt_pknorm_i16_f32 v9, v230, v231
	v_rcp_f32_e32 v3, v13
	v_cmp_lt_f32_e32 vcc, 0, v13
	s_mov_b64 s[6:7], 0x6400
	v_lshl_add_u64 v[10:11], v[4:5], 0, s[6:7]
	v_cndmask_b32_e32 v3, 0, v3, vcc
	global_store_dwordx4 v[10:11], v[6:9], off sc0 sc1
	v_pk_mul_f32 v[224:225], v[34:35], v[2:3] op_sel:[0,1] op_sel_hi:[1,1]
	v_pk_mul_f32 v[226:227], v[36:37], v[2:3] op_sel:[0,1] op_sel_hi:[1,1]
	v_cvt_pknorm_i16_f32 v6, v224, v225
	v_cvt_pknorm_i16_f32 v7, v226, v227
	v_pk_mul_f32 v[228:229], v[38:39], v[2:3] op_sel:[0,1] op_sel_hi:[1,1]
	v_pk_mul_f32 v[230:231], v[40:41], v[2:3] op_sel:[0,1] op_sel_hi:[1,1]
	v_cvt_pknorm_i16_f32 v8, v228, v229
	s_mov_b64 s[6:7], 0x6600
	v_cvt_pknorm_i16_f32 v9, v230, v231
	v_lshl_add_u64 v[10:11], v[4:5], 0, s[6:7]
	global_store_dwordx4 v[10:11], v[6:9], off sc0 sc1
	s_nop 1
	v_pk_mul_f32 v[6:7], v[12:13], s[4:5] op_sel_hi:[1,0]
	global_store_dwordx2 v0, v[6:7], s[2:3] offset:200
	v_accvgpr_read_b32 v3, a252
	v_accvgpr_read_b32 v6, a236
	v_accvgpr_read_b32 v7, a220
	v_max3_f32 v8, |v3|, |v6|, |v7|
	v_accvgpr_read_b32 v9, a204
	v_accvgpr_read_b32 v14, a188
	v_max3_f32 v8, |v8|, |v9|, |v14|
	v_accvgpr_read_b32 v15, a172
	v_accvgpr_read_b32 v16, a156
	v_max3_f32 v8, |v8|, |v15|, |v16|
	v_accvgpr_read_b32 v10, a108
	v_accvgpr_read_b32 v17, a108
	v_max3_f32 v8, |v8|, |v17|, |v10|
	v_accvgpr_read_b32 v18, a253
	v_accvgpr_read_b32 v19, a237
	v_accvgpr_read_b32 v20, a221
	v_max3_f32 v10, |v18|, |v19|, |v20|
	v_accvgpr_read_b32 v21, a205
	v_accvgpr_read_b32 v22, a189
	v_max3_f32 v10, |v10|, |v21|, |v22|
	v_accvgpr_read_b32 v23, a173
	v_accvgpr_read_b32 v24, a157
	v_max3_f32 v10, |v10|, |v23|, |v24|
	v_accvgpr_read_b32 v25, a109
	v_max3_f32 v11, |v10|, |v25|, |v25|
	v_accvgpr_read_b32 v26, a254
	v_accvgpr_read_b32 v27, a238
	v_accvgpr_read_b32 v28, a222
	v_max3_f32 v10, |v26|, |v27|, |v28|
	v_accvgpr_read_b32 v29, a206
	v_accvgpr_read_b32 v30, a190
	v_max3_f32 v10, |v10|, |v29|, |v30|
	v_accvgpr_read_b32 v31, a174
	v_accvgpr_read_b32 v32, a158
	v_max3_f32 v10, |v10|, |v31|, |v32|
	v_accvgpr_read_b32 v33, a110
	v_max3_f32 v12, |v10|, |v33|, |v33|
	v_accvgpr_read_b32 v34, a255
	v_accvgpr_read_b32 v35, a239
	v_accvgpr_read_b32 v36, a223
	v_max3_f32 v10, |v34|, |v35|, |v36|
	v_accvgpr_read_b32 v37, a207
	v_accvgpr_read_b32 v38, a191
	v_max3_f32 v10, |v10|, |v37|, |v38|
	v_accvgpr_read_b32 v39, a175
	v_accvgpr_read_b32 v40, a159
	v_max3_f32 v10, |v10|, |v39|, |v40|
	v_accvgpr_read_b32 v41, a111
	v_max3_f32 v13, |v10|, |v41|, |v41|
	s_mov_b64 s[6:7], 0x7000
	s_nop 1
	v_max_f32_dpp v8, v8, v8 quad_perm:[1,0,3,2] row_mask:0xf bank_mask:0xf
	v_max_f32_dpp v11, v11, v11 quad_perm:[1,0,3,2] row_mask:0xf bank_mask:0xf
	v_max_f32_dpp v12, v12, v12 quad_perm:[1,0,3,2] row_mask:0xf bank_mask:0xf
	v_max_f32_dpp v13, v13, v13 quad_perm:[1,0,3,2] row_mask:0xf bank_mask:0xf
	v_max_f32_dpp v8, v8, v8 quad_perm:[2,3,0,1] row_mask:0xf bank_mask:0xf
	v_max_f32_dpp v11, v11, v11 quad_perm:[2,3,0,1] row_mask:0xf bank_mask:0xf
	v_max_f32_dpp v12, v12, v12 quad_perm:[2,3,0,1] row_mask:0xf bank_mask:0xf
	v_max_f32_dpp v13, v13, v13 quad_perm:[2,3,0,1] row_mask:0xf bank_mask:0xf
	v_max_f32_dpp v8, v8, v8 row_half_mirror row_mask:0xf bank_mask:0xf
	v_max_f32_dpp v11, v11, v11 row_half_mirror row_mask:0xf bank_mask:0xf
	v_max_f32_dpp v12, v12, v12 row_half_mirror row_mask:0xf bank_mask:0xf
	v_max_f32_dpp v13, v13, v13 row_half_mirror row_mask:0xf bank_mask:0xf
	v_max_f32_dpp v8, v8, v8 row_mirror row_mask:0xf bank_mask:0xf
	v_max_f32_dpp v11, v11, v11 row_mirror row_mask:0xf bank_mask:0xf
	v_max_f32_dpp v12, v12, v12 row_mirror row_mask:0xf bank_mask:0xf
	v_max_f32_dpp v13, v13, v13 row_mirror row_mask:0xf bank_mask:0xf
	s_nop 0
	ds_swizzle_b32 v232, v8 offset:swizzle(SWAP,16)
	ds_swizzle_b32 v233, v11 offset:swizzle(SWAP,16)
	ds_swizzle_b32 v234, v12 offset:swizzle(SWAP,16)
	ds_swizzle_b32 v235, v13 offset:swizzle(SWAP,16)
	s_waitcnt lgkmcnt(0)
	v_max_f32_e32 v10, v8, v232
	v_rcp_f32_e32 v8, v10
	v_cmp_lt_f32_e32 vcc, 0, v10
	s_waitcnt lgkmcnt(0)
	v_max_f32_e32 v11, v11, v233
	s_waitcnt lgkmcnt(0)
	v_max_f32_e32 v12, v12, v234
	v_cndmask_b32_e32 v42, 0, v8, vcc
	v_mul_f32_e32 v3, v42, v3
	v_mul_f32_e32 v6, v42, v6
	v_cvt_pknorm_i16_f32 v6, v3, v6
	v_mul_f32_e32 v3, v42, v7
	v_mul_f32_e32 v7, v42, v9
	v_cvt_pknorm_i16_f32 v7, v3, v7
	v_pk_mul_f32 v[224:225], v[14:15], v[42:43] op_sel_hi:[1,0]
	v_pk_mul_f32 v[226:227], v[16:17], v[42:43] op_sel_hi:[1,0]
	v_cvt_pknorm_i16_f32 v8, v224, v225
	v_cvt_pknorm_i16_f32 v9, v226, v227
	v_rcp_f32_e32 v3, v11
	v_cmp_lt_f32_e32 vcc, 0, v11
	v_lshl_add_u64 v[14:15], v[4:5], 0, s[6:7]
	global_store_dwordx4 v[14:15], v[6:9], off sc0 sc1
	s_mov_b64 s[6:7], 0x7200
	v_cndmask_b32_e32 v3, 0, v3, vcc
	v_pk_mul_f32 v[228:229], v[18:19], v[2:3] op_sel:[0,1] op_sel_hi:[1,1]
	v_pk_mul_f32 v[230:231], v[20:21], v[2:3] op_sel:[0,1] op_sel_hi:[1,1]
	v_cvt_pknorm_i16_f32 v6, v228, v229
	v_cvt_pknorm_i16_f32 v7, v230, v231
	v_pk_mul_f32 v[224:225], v[22:23], v[2:3] op_sel:[0,1] op_sel_hi:[1,1]
	v_pk_mul_f32 v[226:227], v[24:25], v[2:3] op_sel:[0,1] op_sel_hi:[1,1]
	v_cvt_pknorm_i16_f32 v8, v224, v225
	v_cvt_pknorm_i16_f32 v9, v226, v227
	v_rcp_f32_e32 v3, v12
	v_cmp_lt_f32_e32 vcc, 0, v12
	v_lshl_add_u64 v[14:15], v[4:5], 0, s[6:7]
	global_store_dwordx4 v[14:15], v[6:9], off sc0 sc1
	s_nop 1
	v_pk_mul_f32 v[6:7], v[10:11], s[4:5] op_sel_hi:[1,0]
	v_cndmask_b32_e32 v3, 0, v3, vcc
	global_store_dwordx2 v0, v[6:7], s[2:3] offset:224
	v_pk_mul_f32 v[228:229], v[26:27], v[2:3] op_sel:[0,1] op_sel_hi:[1,1]
	v_pk_mul_f32 v[230:231], v[28:29], v[2:3] op_sel:[0,1] op_sel_hi:[1,1]
	v_cvt_pknorm_i16_f32 v6, v228, v229
	v_cvt_pknorm_i16_f32 v7, v230, v231
	v_pk_mul_f32 v[224:225], v[30:31], v[2:3] op_sel:[0,1] op_sel_hi:[1,1]
	v_pk_mul_f32 v[226:227], v[32:33], v[2:3] op_sel:[0,1] op_sel_hi:[1,1]
	v_cvt_pknorm_i16_f32 v8, v224, v225
	s_waitcnt lgkmcnt(0)
	v_max_f32_e32 v13, v13, v235
	v_cvt_pknorm_i16_f32 v9, v226, v227
	v_rcp_f32_e32 v3, v13
	v_cmp_lt_f32_e32 vcc, 0, v13
	s_mov_b64 s[6:7], 0x7400
	v_lshl_add_u64 v[10:11], v[4:5], 0, s[6:7]
	v_cndmask_b32_e32 v3, 0, v3, vcc
	global_store_dwordx4 v[10:11], v[6:9], off sc0 sc1
	v_pk_mul_f32 v[228:229], v[34:35], v[2:3] op_sel:[0,1] op_sel_hi:[1,1]
	v_pk_mul_f32 v[230:231], v[36:37], v[2:3] op_sel:[0,1] op_sel_hi:[1,1]
	v_cvt_pknorm_i16_f32 v6, v228, v229
	v_cvt_pknorm_i16_f32 v7, v230, v231
	v_pk_mul_f32 v[224:225], v[38:39], v[2:3] op_sel:[0,1] op_sel_hi:[1,1]
	v_pk_mul_f32 v[226:227], v[40:41], v[2:3] op_sel:[0,1] op_sel_hi:[1,1]
	v_cvt_pknorm_i16_f32 v8, v224, v225
	s_mov_b64 s[6:7], 0x7600
	v_cvt_pknorm_i16_f32 v9, v226, v227
	v_lshl_add_u64 v[4:5], v[4:5], 0, s[6:7]
	global_store_dwordx4 v[4:5], v[6:9], off sc0 sc1
	v_pk_mul_f32 v[4:5], v[12:13], s[4:5] op_sel_hi:[1,0]
	global_store_dwordx2 v0, v[4:5], s[2:3] offset:232
	ds_bpermute_b32 v4, v133, v134
	s_lshl_b64 s[0:1], s[0:1], 2
	s_add_u32 s0, s26, s0
	s_addc_u32 s1, s27, s1
	v_mov_b32_e32 v3, v1
	v_cmp_gt_i32_e32 vcc, 32, v132
	v_lshl_add_u64 v[0:1], s[0:1], 0, v[2:3]
	s_and_saveexec_b64 s[0:1], vcc
	s_cbranch_execz .LBB1_6
	s_waitcnt lgkmcnt(0)
	v_add_f32_e32 v2, v134, v4
	global_store_dword v[0:1], v2, off

_Z7k_graphPKfS0_S0_S0_S0_S0_S0_S0_S0_PfS1_:
	s_load_dwordx2 s[4:5], s[0:1], 0x0
	s_load_dwordx2 s[20:21], s[0:1], 0x8
	s_load_dwordx2 s[22:23], s[0:1], 0x28
	v_lshl_or_b32 v4, s2, 8, v0
	v_add_u32_e32 v2, 0x808, v4
	v_ashrrev_i32_e32 v3, 31, v2
	v_ashrrev_i32_e32 v5, 31, v4
	s_waitcnt lgkmcnt(0)
	v_lshlrev_b32_e32 v122, 4, v0
	v_mov_b32_e32 v123, 0
	v_lshl_add_u64 v[186:187], s[20:21], 0, v[122:123]
	global_load_dwordx4 v[126:129], v122, s[20:21]
	s_movk_i32 s24, 0x2000
	v_add_co_u32_e32 v138, vcc, s24, v186
	s_movk_i32 s25, 0x3000
	s_nop 0
	v_addc_co_u32_e32 v139, vcc, 0, v187, vcc
	global_load_dwordx4 v[130:133], v[138:139], off offset:-4096
	global_load_dwordx4 v[134:137], v[138:139], off
	v_add_co_u32_e32 v146, vcc, s25, v186
	v_or_b32_e32 v224, 0x400, v0
	s_nop 0
	v_addc_co_u32_e32 v147, vcc, 0, v187, vcc
	v_lshlrev_b32_e32 v206, 4, v224
	global_load_dwordx4 v[138:141], v[146:147], off
	global_load_dwordx4 v[142:145], v206, s[20:21]
	s_movk_i32 s26, 0x6000
	v_add_co_u32_e32 v154, vcc, s26, v186
	s_movk_i32 s27, 0x7000
	s_nop 0
	v_addc_co_u32_e32 v155, vcc, 0, v187, vcc
	global_load_dwordx4 v[146:149], v[154:155], off offset:-4096
	global_load_dwordx4 v[150:153], v[154:155], off
	v_add_co_u32_e32 v162, vcc, s27, v186
	v_or_b32_e32 v228, 0x800, v0
	s_nop 0
	v_addc_co_u32_e32 v163, vcc, 0, v187, vcc
	v_lshlrev_b32_e32 v164, 4, v228
	global_load_dwordx4 v[154:157], v[162:163], off
	global_load_dwordx4 v[158:161], v164, s[20:21]
	s_mov_b32 s28, 0xa000
	v_add_co_u32_e32 v170, vcc, s28, v186
	s_mov_b32 s28, 0xb000
	s_nop 0
	v_addc_co_u32_e32 v171, vcc, 0, v187, vcc
	global_load_dwordx4 v[162:165], v[170:171], off offset:-4096
	global_load_dwordx4 v[166:169], v[170:171], off
	v_add_co_u32_e32 v178, vcc, s28, v186
	v_or_b32_e32 v231, 0xc00, v0
	s_nop 0
	v_addc_co_u32_e32 v179, vcc, 0, v187, vcc
	v_lshlrev_b32_e32 v180, 4, v231
	global_load_dwordx4 v[170:173], v[178:179], off
	global_load_dwordx4 v[174:177], v180, s[20:21]
	s_mov_b32 s29, 0xe000
	v_add_co_u32_e32 v188, vcc, s29, v186
	s_mov_b32 s29, 0xf000
	s_nop 0
	v_addc_co_u32_e32 v189, vcc, 0, v187, vcc
	global_load_dwordx4 v[178:181], v[188:189], off offset:-4096
	global_load_dwordx4 v[182:185], v[188:189], off
	v_add_co_u32_e32 v186, vcc, s29, v186
	v_lshl_add_u64 v[218:219], s[22:23], 0, v[122:123]
	s_nop 0
	v_addc_co_u32_e32 v187, vcc, 0, v187, vcc
	global_load_dwordx4 v[186:189], v[186:187], off
	v_add_co_u32_e32 v198, vcc, s24, v218
	global_load_dwordx4 v[190:193], v122, s[22:23]
	s_nop 0
	v_addc_co_u32_e32 v199, vcc, 0, v219, vcc
	global_load_dwordx4 v[194:197], v[198:199], off offset:-4096
	v_add_co_u32_e32 v202, vcc, s25, v218
	global_load_dwordx4 v[206:209], v206, s[22:23]
	s_nop 0
	v_addc_co_u32_e32 v203, vcc, 0, v219, vcc
	global_load_dwordx4 v[202:205], v[202:203], off
	v_add_co_u32_e32 v214, vcc, s26, v218
	global_load_dwordx4 v[198:201], v[198:199], off
	s_nop 0
	v_addc_co_u32_e32 v215, vcc, 0, v219, vcc
	global_load_dwordx4 v[210:213], v[214:215], off offset:-4096
	v_add_co_u32_e32 v218, vcc, s27, v218
	global_load_dwordx4 v[214:217], v[214:215], off
	s_nop 0
	v_addc_co_u32_e32 v219, vcc, 0, v219, vcc
	global_load_dwordx4 v[218:221], v[218:219], off
	v_lshl_add_u64 v[10:11], v[2:3], 2, s[4:5]
	v_add_u32_e32 v2, 0x1010, v4
	v_ashrrev_i32_e32 v3, 31, v2
	v_lshl_add_u64 v[12:13], v[2:3], 2, s[4:5]
	v_add_u32_e32 v2, 0x1818, v4
	v_lshl_add_u64 v[8:9], v[4:5], 2, s[4:5]
	v_ashrrev_i32_e32 v3, 31, v2
	v_lshl_add_u64 v[14:15], v[2:3], 2, s[4:5]
	global_load_dword v6, v[8:9], off
	global_load_dword v5, v[10:11], off
	global_load_dword v3, v[12:13], off
	global_load_dword v2, v[14:15], off
	v_add_u32_e32 v8, 0x2020, v4
	v_ashrrev_i32_e32 v9, 31, v8
	v_lshl_add_u64 v[12:13], v[8:9], 2, s[4:5]
	v_add_u32_e32 v8, 0x2828, v4
	v_ashrrev_i32_e32 v9, 31, v8
	v_lshl_add_u64 v[14:15], v[8:9], 2, s[4:5]
	v_add_u32_e32 v8, 0x3030, v4
	v_ashrrev_i32_e32 v9, 31, v8
	v_lshl_add_u64 v[16:17], v[8:9], 2, s[4:5]
	v_add_u32_e32 v8, 0x3838, v4
	v_ashrrev_i32_e32 v9, 31, v8
	v_lshl_add_u64 v[18:19], v[8:9], 2, s[4:5]
	global_load_dword v10, v[12:13], off
	global_load_dword v9, v[14:15], off
	global_load_dword v8, v[16:17], off
	global_load_dword v7, v[18:19], off
	s_add_i32 s6, s2, 0x800
	s_ashr_i32 s7, s6, 31
	s_lshl_b64 s[6:7], s[6:7], 2
	s_add_u32 s6, s4, s6
	s_addc_u32 s7, s5, s7
	s_add_i32 s8, s2, 0x1008
	s_ashr_i32 s9, s8, 31
	s_lshl_b64 s[8:9], s[8:9], 2
	s_add_u32 s12, s4, s8
	s_addc_u32 s13, s5, s9
	s_add_i32 s8, s2, 0x1810
	s_ashr_i32 s9, s8, 31
	s_lshl_b64 s[8:9], s[8:9], 2
	s_add_u32 s14, s4, s8
	s_addc_u32 s15, s5, s9
	s_add_i32 s8, s2, 0x2018
	s_ashr_i32 s9, s8, 31
	s_lshl_b64 s[8:9], s[8:9], 2
	s_add_u32 s16, s4, s8
	s_addc_u32 s17, s5, s9
	s_load_dword s10, s[6:7], 0x0
	s_load_dword s9, s[12:13], 0x0
	s_load_dword s8, s[14:15], 0x0
	s_load_dword s3, s[16:17], 0x0
	s_add_i32 s6, s2, 0x2820
	s_ashr_i32 s7, s6, 31
	s_lshl_b64 s[6:7], s[6:7], 2
	s_add_u32 s6, s4, s6
	s_addc_u32 s7, s5, s7
	s_add_i32 s12, s2, 0x3028
	s_ashr_i32 s13, s12, 31
	s_lshl_b64 s[12:13], s[12:13], 2
	s_add_u32 s12, s4, s12
	s_addc_u32 s13, s5, s13
	s_add_i32 s14, s2, 0x3830
	s_ashr_i32 s15, s14, 31
	s_lshl_b64 s[14:15], s[14:15], 2
	s_add_u32 s14, s4, s14
	s_addc_u32 s15, s5, s15
	s_add_i32 s16, s2, 0x4038
	s_ashr_i32 s17, s16, 31
	s_lshl_b64 s[16:17], s[16:17], 2
	s_add_u32 s4, s4, s16
	s_addc_u32 s5, s5, s17
	s_load_dword s18, s[6:7], 0x0
	s_load_dword s16, s[12:13], 0x0
	s_load_dword s11, s[14:15], 0x0
	s_load_dword s17, s[4:5], 0x0
	s_movk_i32 s4, 0xbf
	v_mov_b32_e32 v11, 0
	v_cmp_lt_u32_e32 vcc, s4, v0
	s_and_saveexec_b64 s[4:5], vcc
	s_xor_b64 s[4:5], exec, s[4:5]
	s_cbranch_execz .LBB2_4
	s_movk_i32 s6, 0xe0
	v_cmp_gt_u32_e32 vcc, s6, v0
	s_and_saveexec_b64 s[6:7], vcc
	s_cbranch_execz .LBB2_3
	s_load_dwordx2 s[12:13], s[0:1], 0x38
	v_lshlrev_b32_e32 v1, 2, v0
	s_waitcnt lgkmcnt(0)
	global_load_dword v11, v1, s[12:13] offset:-768

.LBB2_12:
	s_or_b64 exec, exec, s[4:5]
	s_waitcnt vmcnt(7)
	v_add_f32_e32 v6, 0, v6
	s_waitcnt lgkmcnt(0)
	v_add_f32_e64 v12, s10, 0
	s_waitcnt vmcnt(6)
	v_add_f32_e32 v5, v6, v5
	v_add_f32_e32 v6, s9, v12
	s_waitcnt vmcnt(5)
	v_add_f32_e32 v3, v5, v3
	v_add_f32_e32 v5, s8, v6
	s_waitcnt vmcnt(4)
	v_add_f32_e32 v2, v3, v2
	v_add_f32_e32 v3, s3, v5
	v_add_f32_e32 v3, s18, v3
	s_waitcnt vmcnt(3)
	v_add_f32_e32 v2, v2, v10
	v_add_f32_e32 v3, s16, v3
	s_waitcnt vmcnt(2)
	v_add_f32_e32 v2, v2, v9
	v_add_f32_e32 v3, s11, v3
	s_waitcnt vmcnt(1)
	v_add_f32_e32 v2, v2, v8
	v_add_f32_e32 v3, s17, v3
	s_waitcnt vmcnt(0)
	v_add_f32_e32 v2, v2, v7
	v_max_f32_e32 v3, 1.0, v3
	v_div_scale_f32 v5, s[4:5], v3, v3, v2
	v_rcp_f32_e32 v6, v5
	s_movk_i32 s3, 0xe0
	v_fma_f32 v7, -v5, v6, 1.0
	v_fmac_f32_e32 v6, v7, v6
	v_div_scale_f32 v7, vcc, v2, v3, v2
	v_mul_f32_e32 v8, v7, v6
	v_fma_f32 v9, -v5, v8, v7
	v_fmac_f32_e32 v8, v9, v6
	v_fma_f32 v5, -v5, v8, v7
	v_div_fmas_f32 v5, v5, v6, v8
	v_div_fixup_f32 v2, v5, v3, v2
	v_mov_b32_e32 v3, 0x18000
	v_lshl_or_b32 v3, v0, 2, v3
	v_cmp_gt_u32_e32 vcc, s3, v0
	ds_write_b32 v3, v2
	s_and_saveexec_b64 s[4:5], vcc
	v_mov_b32_e32 v2, 0x18800
	v_lshl_or_b32 v2, v0, 2, v2
	ds_write_b32 v2, v11
	s_or_b64 exec, exec, s[4:5]
	v_lshlrev_b32_e32 v2, 4, v0
	v_mov_b32_e32 v3, 0
	s_load_dwordx2 s[10:11], s[0:1], 0x50
	s_load_dwordx4 s[4:7], s[0:1], 0x40
	s_load_dwordx2 s[8:9], s[0:1], 0x20
	v_or_b32_e32 v104, 0x400, v0
	v_or_b32_e32 v108, 0x800, v0
	v_or_b32_e32 v111, 0xc00, v0
	v_and_b32_e32 v116, 0xf0, v2
	v_lshrrev_b32_e32 v117, 4, v0
	s_movk_i32 s0, 0x180
	v_or_b32_e32 v5, 0x100, v0
	v_mad_u32_u24 v117, v117, s0, v116
	s_waitcnt vmcnt(23)
	ds_write_b128 v117, v[126:129]
	v_lshrrev_b32_e32 v6, 4, v5
	v_or_b32_e32 v102, 0x200, v0
	v_mad_u32_u24 v6, v6, s0, v116
	s_waitcnt vmcnt(22)
	ds_write_b128 v6, v[130:133]
	v_lshrrev_b32_e32 v6, 4, v102
	v_or_b32_e32 v103, 0x300, v0
	v_mad_u32_u24 v6, v6, s0, v116
	s_waitcnt vmcnt(21)
	ds_write_b128 v6, v[134:137]
	v_lshrrev_b32_e32 v6, 4, v103
	v_mad_u32_u24 v6, v6, s0, v116
	s_waitcnt vmcnt(20)
	ds_write_b128 v6, v[138:141]
	v_lshrrev_b32_e32 v6, 4, v104
	v_or_b32_e32 v105, 0x500, v0
	v_mad_u32_u24 v6, v6, s0, v116
	s_waitcnt vmcnt(19)
	ds_write_b128 v6, v[142:145]
	v_lshrrev_b32_e32 v6, 4, v105
	v_or_b32_e32 v106, 0x600, v0
	v_mad_u32_u24 v6, v6, s0, v116
	s_waitcnt vmcnt(18)
	ds_write_b128 v6, v[146:149]
	v_lshrrev_b32_e32 v6, 4, v106
	v_or_b32_e32 v107, 0x700, v0
	v_mad_u32_u24 v6, v6, s0, v116
	s_waitcnt vmcnt(17)
	ds_write_b128 v6, v[150:153]
	v_lshrrev_b32_e32 v6, 4, v107
	v_mad_u32_u24 v6, v6, s0, v116
	s_waitcnt vmcnt(16)
	ds_write_b128 v6, v[154:157]
	v_lshrrev_b32_e32 v6, 4, v108
	v_or_b32_e32 v109, 0x900, v0
	v_mad_u32_u24 v6, v6, s0, v116
	s_waitcnt vmcnt(15)
	ds_write_b128 v6, v[158:161]
	v_lshrrev_b32_e32 v6, 4, v109
	v_or_b32_e32 v110, 0xa00, v0
	v_mad_u32_u24 v6, v6, s0, v116
	s_waitcnt vmcnt(14)
	ds_write_b128 v6, v[162:165]
	v_lshrrev_b32_e32 v6, 4, v110
	v_or_b32_e32 v112, 0xb00, v0
	v_mad_u32_u24 v6, v6, s0, v116
	s_waitcnt vmcnt(13)
	ds_write_b128 v6, v[166:169]
	v_lshrrev_b32_e32 v6, 4, v112
	v_mad_u32_u24 v6, v6, s0, v116
	s_waitcnt vmcnt(12)
	ds_write_b128 v6, v[170:173]
	v_lshrrev_b32_e32 v6, 4, v111
	v_or_b32_e32 v113, 0xd00, v0
	v_mad_u32_u24 v6, v6, s0, v116
	s_waitcnt vmcnt(11)
	ds_write_b128 v6, v[174:177]
	v_lshrrev_b32_e32 v6, 4, v113
	v_or_b32_e32 v114, 0xe00, v0
	v_mad_u32_u24 v6, v6, s0, v116
	s_waitcnt vmcnt(10)
	ds_write_b128 v6, v[178:181]
	v_lshrrev_b32_e32 v6, 4, v114
	v_or_b32_e32 v115, 0xf00, v0
	v_mad_u32_u24 v6, v6, s0, v116
	s_waitcnt vmcnt(9)
	ds_write_b128 v6, v[182:185]
	v_lshrrev_b32_e32 v6, 4, v115
	v_mad_u32_u24 v6, v6, s0, v116
	s_waitcnt vmcnt(8)
	ds_write_b128 v6, v[186:189]
	v_lshrrev_b32_e32 v6, 3, v0
	v_lshrrev_b32_e32 v5, 3, v5
	v_mul_u32_u24_e32 v6, 0x180, v6
	v_and_b32_e32 v2, 0x70, v2
	v_mul_u32_u24_e32 v5, 0x180, v5
	v_or_b32_e32 v6, v6, v2
	v_or_b32_e32 v5, v5, v2
	s_waitcnt vmcnt(7)
	ds_write_b128 v6, v[190:193] offset:256
	s_waitcnt vmcnt(6)
	ds_write_b128 v5, v[194:197] offset:256
	v_lshrrev_b32_e32 v5, 3, v102
	v_mul_u32_u24_e32 v5, 0x180, v5
	v_or_b32_e32 v5, v5, v2
	s_waitcnt vmcnt(3)
	ds_write_b128 v5, v[198:201] offset:256
	v_lshrrev_b32_e32 v5, 3, v103
	v_mul_u32_u24_e32 v5, 0x180, v5
	v_or_b32_e32 v5, v5, v2
	ds_write_b128 v5, v[202:205] offset:256
	v_lshrrev_b32_e32 v5, 3, v104
	v_mul_u32_u24_e32 v5, 0x180, v5
	v_or_b32_e32 v5, v5, v2
	ds_write_b128 v5, v[206:209] offset:256
	v_lshrrev_b32_e32 v5, 3, v105
	v_mul_u32_u24_e32 v5, 0x180, v5
	v_or_b32_e32 v5, v5, v2
	s_waitcnt vmcnt(2)
	ds_write_b128 v5, v[210:213] offset:256
	v_lshrrev_b32_e32 v5, 3, v106
	v_mul_u32_u24_e32 v5, 0x180, v5
	v_or_b32_e32 v5, v5, v2
	s_waitcnt vmcnt(1)
	ds_write_b128 v5, v[214:217] offset:256
	v_lshrrev_b32_e32 v5, 3, v107
	v_mul_u32_u24_e32 v5, 0x180, v5
	v_or_b32_e32 v2, v5, v2
	s_waitcnt vmcnt(0)
	ds_write_b128 v2, v[218:221] offset:256
	v_and_b32_e32 v2, 0x7f, v0
	v_lshrrev_b32_e32 v7, 7, v0
	s_movk_i32 s0, 0x60
	v_cmp_gt_u32_e32 vcc, s0, v2
	v_lshlrev_b32_e32 v5, 9, v7
	s_waitcnt lgkmcnt(0)
	s_barrier
	s_and_saveexec_b64 s[0:1], vcc
	s_cbranch_execz .LBB2_18
	v_and_b32_e32 v3, 0x80, v0
	v_or_b32_e32 v6, 0x7f, v0
	v_sub_u32_e32 v3, v6, v3
	v_add_u32_e32 v6, 1, v3
	v_mul_u32_u24_e32 v3, 0xc000, v7
	v_lshl_or_b32 v7, v2, 2, v3
	v_mov_b32_e32 v3, 0
	s_mov_b64 s[12:13], 0
	v_mov_b32_e32 v8, v5

	.amdhsa_kernel _Z7k_graphPKfS0_S0_S0_S0_S0_S0_S0_S0_PfS1_
		.amdhsa_group_segment_fixed_size 101632
		.amdhsa_private_segment_fixed_size 0
		.amdhsa_kernarg_size 88
		.amdhsa_user_sgpr_count 2
		.amdhsa_user_sgpr_dispatch_ptr 0
		.amdhsa_user_sgpr_queue_ptr 0
		.amdhsa_user_sgpr_kernarg_segment_ptr 1
		.amdhsa_user_sgpr_dispatch_id 0
		.amdhsa_user_sgpr_kernarg_preload_length 0
		.amdhsa_user_sgpr_kernarg_preload_offset 0
		.amdhsa_user_sgpr_private_segment_size 0
		.amdhsa_uses_dynamic_stack 0
		.amdhsa_enable_private_segment 0
		.amdhsa_system_sgpr_workgroup_id_x 1
		.amdhsa_system_sgpr_workgroup_id_y 0
		.amdhsa_system_sgpr_workgroup_id_z 0
		.amdhsa_system_sgpr_workgroup_info 0
		.amdhsa_system_vgpr_workitem_id 0
		.amdhsa_next_free_vgpr 257
		.amdhsa_next_free_sgpr 96
		.amdhsa_accum_offset 236
		.amdhsa_reserve_vcc 1
		.amdhsa_float_round_mode_32 0
		.amdhsa_float_round_mode_16_64 0
		.amdhsa_float_denorm_mode_32 3
		.amdhsa_float_denorm_mode_16_64 3
		.amdhsa_dx10_clamp 1
		.amdhsa_ieee_mode 1
		.amdhsa_fp16_overflow 0
		.amdhsa_tg_split 0
		.amdhsa_exception_fp_ieee_invalid_op 0
		.amdhsa_exception_fp_denorm_src 0
		.amdhsa_exception_fp_ieee_div_zero 0
		.amdhsa_exception_fp_ieee_overflow 0
		.amdhsa_exception_fp_ieee_underflow 0
		.amdhsa_exception_fp_ieee_inexact 0
		.amdhsa_exception_int_div_zero 0
	.end_amdhsa_kernel

amdhsa.kernels:
  - .agpr_count:     0
    .args:
      - .actual_access:  read_only
        .address_space:  global
        .offset:         0
        .size:           8
        .value_kind:     global_buffer
      - .address_space:  global
        .offset:         8
        .size:           8
        .value_kind:     global_buffer
      - .actual_access:  read_only
        .address_space:  global
        .offset:         16
        .size:           8
        .value_kind:     global_buffer
      - .actual_access:  read_only
        .address_space:  global
        .offset:         24
        .size:           8
        .value_kind:     global_buffer
      - .actual_access:  read_only
        .address_space:  global
        .offset:         32
        .size:           8
        .value_kind:     global_buffer
      - .actual_access:  read_only
        .address_space:  global
        .offset:         40
        .size:           8
        .value_kind:     global_buffer
      - .actual_access:  read_only
        .address_space:  global
        .offset:         48
        .size:           8
        .value_kind:     global_buffer
      - .actual_access:  read_only
        .address_space:  global
        .offset:         56
        .size:           8
        .value_kind:     global_buffer
      - .actual_access:  write_only
        .address_space:  global
        .offset:         64
        .size:           8
        .value_kind:     global_buffer
      - .actual_access:  write_only
        .address_space:  global
        .offset:         72
        .size:           8
        .value_kind:     global_buffer
      - .actual_access:  write_only
        .address_space:  global
        .offset:         80
        .size:           8
        .value_kind:     global_buffer
      - .actual_access:  write_only
        .address_space:  global
        .offset:         88
        .size:           8
        .value_kind:     global_buffer
      - .actual_access:  read_only
        .address_space:  global
        .offset:         96
        .size:           8
        .value_kind:     global_buffer
      - .actual_access:  write_only
        .address_space:  global
        .offset:         104
        .size:           8
        .value_kind:     global_buffer
      - .actual_access:  read_only
        .address_space:  global
        .offset:         112
        .size:           8
        .value_kind:     global_buffer
      - .actual_access:  write_only
        .address_space:  global
        .offset:         120
        .size:           8
        .value_kind:     global_buffer
      - .actual_access:  write_only
        .address_space:  global
        .offset:         128
        .size:           8
        .value_kind:     global_buffer
      - .actual_access:  write_only
        .address_space:  global
        .offset:         136
        .size:           8
        .value_kind:     global_buffer
      - .actual_access:  write_only
        .address_space:  global
        .offset:         144
        .size:           8
        .value_kind:     global_buffer
    .group_segment_fixed_size: 4096
    .kernarg_segment_align: 8
    .kernarg_segment_size: 152
    .language:       OpenCL C
    .language_version:
      - 2
      - 0
    .max_flat_workgroup_size: 512
    .name:           _Z7k_frontPKfPmS0_S0_S0_S0_S0_S0_PDF16_S2_PfS3_S0_S2_S0_S2_S3_S3_S3_
    .private_segment_fixed_size: 0
    .sgpr_count:     88
    .sgpr_spill_count: 0
    .symbol:         _Z7k_frontPKfPmS0_S0_S0_S0_S0_S0_PDF16_S2_PfS3_S0_S2_S0_S2_S3_S3_S3_.kd
    .uniform_work_group_size: 1
    .uses_dynamic_stack: false
    .vgpr_count:     68
    .vgpr_spill_count: 0
    .wavefront_size: 64
  - .agpr_count:     256
    .args:
      - .actual_access:  read_only
        .address_space:  global
        .offset:         0
        .size:           8
        .value_kind:     global_buffer
      - .actual_access:  read_only
        .address_space:  global
        .offset:         8
        .size:           8
        .value_kind:     global_buffer
      - .actual_access:  read_only
        .address_space:  global
        .offset:         16
        .size:           8
        .value_kind:     global_buffer
      - .actual_access:  read_only
        .address_space:  global
        .offset:         24
        .size:           8
        .value_kind:     global_buffer
      - .actual_access:  read_only
        .address_space:  global
        .offset:         32
        .size:           8
        .value_kind:     global_buffer
      - .address_space:  global
        .offset:         40
        .size:           8
        .value_kind:     global_buffer
      - .actual_access:  write_only
        .address_space:  global
        .offset:         48
        .size:           8
        .value_kind:     global_buffer
      - .actual_access:  write_only
        .address_space:  global
        .offset:         56
        .size:           8
        .value_kind:     global_buffer
    .group_segment_fixed_size: 114688
    .kernarg_segment_align: 8
    .kernarg_segment_size: 64
    .language:       OpenCL C
    .language_version:
      - 2
      - 0
    .max_flat_workgroup_size: 256
    .name:           _Z6k_mainPKDF16_PKfS2_S2_PKmPjPfS6_
    .private_segment_fixed_size: 0
    .sgpr_count:     108
    .sgpr_spill_count: 0
    .symbol:         _Z6k_mainPKDF16_PKfS2_S2_PKmPjPfS6_.kd
    .uniform_work_group_size: 1
    .uses_dynamic_stack: false
    .vgpr_count:     492
    .vgpr_spill_count: 0
    .wavefront_size: 64
  - .agpr_count:     0
    .args:
      - .actual_access:  read_only
        .address_space:  global
        .offset:         0
        .size:           8
        .value_kind:     global_buffer
      - .actual_access:  read_only
        .address_space:  global
        .offset:         8
        .size:           8
        .value_kind:     global_buffer
      - .actual_access:  read_only
        .address_space:  global
        .offset:         16
        .size:           8
        .value_kind:     global_buffer
      - .actual_access:  read_only
        .address_space:  global
        .offset:         24
        .size:           8
        .value_kind:     global_buffer
      - .actual_access:  read_only
        .address_space:  global
        .offset:         32
        .size:           8
        .value_kind:     global_buffer
      - .actual_access:  read_only
        .address_space:  global
        .offset:         40
        .size:           8
        .value_kind:     global_buffer
      - .actual_access:  read_only
        .address_space:  global
        .offset:         48
        .size:           8
        .value_kind:     global_buffer
      - .actual_access:  read_only
        .address_space:  global
        .offset:         56
        .size:           8
        .value_kind:     global_buffer
      - .actual_access:  read_only
        .address_space:  global
        .offset:         64
        .size:           8
        .value_kind:     global_buffer
      - .actual_access:  write_only
        .address_space:  global
        .offset:         72
        .size:           8
        .value_kind:     global_buffer
      - .actual_access:  write_only
        .address_space:  global
        .offset:         80
        .size:           8
        .value_kind:     global_buffer
    .group_segment_fixed_size: 101632
    .kernarg_segment_align: 8
    .kernarg_segment_size: 88
    .language:       OpenCL C
    .language_version:
      - 2
      - 0
    .max_flat_workgroup_size: 256
    .name:           _Z7k_graphPKfS0_S0_S0_S0_S0_S0_S0_S0_PfS1_
    .private_segment_fixed_size: 0
    .sgpr_count:     25
    .sgpr_spill_count: 0
    .symbol:         _Z7k_graphPKfS0_S0_S0_S0_S0_S0_S0_S0_PfS1_.kd
    .uniform_work_group_size: 1
    .uses_dynamic_stack: false
    .vgpr_count:     236
    .vgpr_spill_count: 0
    .wavefront_size: 64
  - .agpr_count:     0
    .args:
      - .actual_access:  read_only
        .address_space:  global
        .offset:         0
        .size:           8
        .value_kind:     global_buffer
      - .actual_access:  read_only
        .address_space:  global
        .offset:         8
        .size:           8
        .value_kind:     global_buffer
      - .actual_access:  read_only
        .address_space:  global
        .offset:         16
        .size:           8
        .value_kind:     global_buffer
      - .actual_access:  read_only
        .address_space:  global
        .offset:         24
        .size:           8
        .value_kind:     global_buffer
      - .actual_access:  read_only
        .address_space:  global
        .offset:         32
        .size:           8
        .value_kind:     global_buffer
      - .actual_access:  read_only
        .address_space:  global
        .offset:         40
        .size:           8
        .value_kind:     global_buffer
      - .actual_access:  read_only
        .address_space:  global
        .offset:         48
        .size:           8
        .value_kind:     global_buffer
      - .address_space:  global
        .offset:         56
        .size:           8
        .value_kind:     global_buffer
      - .actual_access:  read_only
        .address_space:  global
        .offset:         64
        .size:           8
        .value_kind:     global_buffer
      - .actual_access:  read_only
        .address_space:  global
        .offset:         72
        .size:           8
        .value_kind:     global_buffer
      - .actual_access:  read_only
        .address_space:  global
        .offset:         80
        .size:           8
        .value_kind:     global_buffer
      - .address_space:  global
        .offset:         88
        .size:           8
        .value_kind:     global_buffer
      - .actual_access:  write_only
        .address_space:  global
        .offset:         96
        .size:           8
        .value_kind:     global_buffer
      - .actual_access:  write_only
        .address_space:  global
        .offset:         104
        .size:           8
        .value_kind:     global_buffer
      - .actual_access:  write_only
        .address_space:  global
        .offset:         112
        .size:           8
        .value_kind:     global_buffer
      - .actual_access:  read_only
        .address_space:  global
        .offset:         120
        .size:           8
        .value_kind:     global_buffer
      - .actual_access:  read_only
        .address_space:  global
        .offset:         128
        .size:           8
        .value_kind:     global_buffer
      - .actual_access:  read_only
        .address_space:  global
        .offset:         136
        .size:           8
        .value_kind:     global_buffer
      - .actual_access:  read_only
        .address_space:  global
        .offset:         144
        .size:           8
        .value_kind:     global_buffer
      - .actual_access:  read_only
        .address_space:  global
        .offset:         152
        .size:           8
        .value_kind:     global_buffer
      - .actual_access:  read_only
        .address_space:  global
        .offset:         160
        .size:           8
        .value_kind:     global_buffer
      - .actual_access:  read_only
        .address_space:  global
        .offset:         168
        .size:           8
        .value_kind:     global_buffer
    .group_segment_fixed_size: 53792
    .kernarg_segment_align: 8
    .kernarg_segment_size: 176
    .language:       OpenCL C
    .language_version:
      - 2
      - 0
    .max_flat_workgroup_size: 512
    .name:           _Z9k_redprepILi1EEvPKfPKjS1_S1_S1_S1_S1_PfPKDv8_DF16_S7_S1_PDF16_S4_S4_S4_PKiS7_S1_S1_S1_S4_S4_
    .private_segment_fixed_size: 0
    .sgpr_count:     106
    .sgpr_spill_count: 4
    .symbol:         _Z9k_redprepILi1EEvPKfPKjS1_S1_S1_S1_S1_PfPKDv8_DF16_S7_S1_PDF16_S4_S4_S4_PKiS7_S1_S1_S1_S4_S4_.kd
    .uniform_work_group_size: 1
    .uses_dynamic_stack: false
    .vgpr_count:     103
    .vgpr_spill_count: 0
    .wavefront_size: 64
  - .agpr_count:     0
    .args:
      - .actual_access:  read_only
        .address_space:  global
        .offset:         0
        .size:           8
        .value_kind:     global_buffer
      - .actual_access:  read_only
        .address_space:  global
        .offset:         8
        .size:           8
        .value_kind:     global_buffer
      - .actual_access:  read_only
        .address_space:  global
        .offset:         16
        .size:           8
        .value_kind:     global_buffer
      - .actual_access:  read_only
        .address_space:  global
        .offset:         24
        .size:           8
        .value_kind:     global_buffer
      - .actual_access:  read_only
        .address_space:  global
        .offset:         32
        .size:           8
        .value_kind:     global_buffer
      - .actual_access:  read_only
        .address_space:  global
        .offset:         40
        .size:           8
        .value_kind:     global_buffer
      - .actual_access:  read_only
        .address_space:  global
        .offset:         48
        .size:           8
        .value_kind:     global_buffer
      - .address_space:  global
        .offset:         56
        .size:           8
        .value_kind:     global_buffer
      - .actual_access:  read_only
        .address_space:  global
        .offset:         64
        .size:           8
        .value_kind:     global_buffer
      - .actual_access:  read_only
        .address_space:  global
        .offset:         72
        .size:           8
        .value_kind:     global_buffer
      - .actual_access:  read_only
        .address_space:  global
        .offset:         80
        .size:           8
        .value_kind:     global_buffer
      - .actual_access:  read_only
        .address_space:  global
        .offset:         88
        .size:           8
        .value_kind:     global_buffer
      - .actual_access:  read_only
        .address_space:  global
        .offset:         96
        .size:           8
        .value_kind:     global_buffer
      - .actual_access:  read_only
        .address_space:  global
        .offset:         104
        .size:           8
        .value_kind:     global_buffer
      - .actual_access:  read_only
        .address_space:  global
        .offset:         112
        .size:           8
        .value_kind:     global_buffer
      - .actual_access:  read_only
        .address_space:  global
        .offset:         120
        .size:           8
        .value_kind:     global_buffer
      - .actual_access:  read_only
        .address_space:  global
        .offset:         128
        .size:           8
        .value_kind:     global_buffer
      - .actual_access:  read_only
        .address_space:  global
        .offset:         136
        .size:           8
        .value_kind:     global_buffer
      - .actual_access:  read_only
        .address_space:  global
        .offset:         144
        .size:           8
        .value_kind:     global_buffer
      - .actual_access:  read_only
        .address_space:  global
        .offset:         152
        .size:           8
        .value_kind:     global_buffer
      - .actual_access:  write_only
        .address_space:  global
        .offset:         160
        .size:           8
        .value_kind:     global_buffer
      - .address_space:  global
        .offset:         168
        .size:           8
        .value_kind:     global_buffer
    .group_segment_fixed_size: 66688
    .kernarg_segment_align: 8
    .kernarg_segment_size: 176
    .language:       OpenCL C
    .language_version:
      - 2
      - 0
    .max_flat_workgroup_size: 512
    .name:           _Z9k_redprepILi2EEvPKfPKjS1_S1_S1_S1_S1_PfPKDv8_DF16_S7_S1_PDF16_S4_S4_S4_PKiS7_S1_S1_S1_S4_S4_
    .private_segment_fixed_size: 0
    .sgpr_count:     102
    .sgpr_spill_count: 0
    .symbol:         _Z9k_redprepILi2EEvPKfPKjS1_S1_S1_S1_S1_PfPKDv8_DF16_S7_S1_PDF16_S4_S4_S4_PKiS7_S1_S1_S1_S4_S4_.kd
    .uniform_work_group_size: 1
    .uses_dynamic_stack: false
    .vgpr_count:     106
    .vgpr_spill_count: 0
    .wavefront_size: 64
